# v056 + nt hint on the even-layer mixer's read-once H row loads (74 global_load_dwordx4)
# speedup vs baseline: 1.0018x; 1.0018x over previous
; __device__ __forceinline__ void unpack8(const u32x4 w, float (&f)[8]) { f[0] = bf_lo(w.x); f[1] = bf_hi(w.x); f[2] = bf_lo(w.y); f[3] = bf_hi(w.y); f[4] = bf_lo(w.z); f[5] = bf_hi(w.z); f[6] = bf_lo(w.w); f[7] = bf_hi(w.w); }
; __global__ void __launch_bounds__(NWAVES * 64, 2) mk_fwd(Args args) {
;     ...
;                     } else {
;                         const int ch0 = 8 * lane;
;                         float w0[8], w1[8], w2[8];
;                         { const f32x4 a0 = *(const f32x4*)(conv_w + ch0), a1 = *(const f32x4*)(conv_w + ch0 + 4), b0 = *(const f32x4*)(conv_w + 512 + ch0), b1 = *(const f32x4*)(conv_w + 512 + ch0 + 4),
;                                       c0 = *(const f32x4*)(conv_w + 1024 + ch0), c1 = *(const f32x4*)(conv_w + 1024 + ch0 + 4);
; #pragma unroll
;                           for (int i = 0; i < 4; ++i) { w0[i] = a0[i]; w0[4 + i] = a1[i]; w1[i] = b0[i]; w1[4 + i] = b1[i]; w2[i] = c0[i]; w2[4 + i] = c1[i]; } }
;                         const bf16_t* pb = hb + 512 + ch0; const bf16_t* pc = hb + 1024 + ch0; const bf16_t* pv = hb + 1536 + ch0;
;                         float up[8], uc[8], un[8];
; #pragma unroll
;                         for (int i = 0; i < 8; ++i) up[i] = 0.f;
;                         if (t0 > 0) { float c[8], v[8]; unpack8(*(const u32x4*)(pc + (size_t)(t0 - 1) * EVEN_IN), c); unpack8(*(const u32x4*)(pv + (size_t)(t0 - 1) * EVEN_IN), v);
; #pragma unroll
;                             for (int i = 0; i < 8; ++i) up[i] = c[i] * v[i]; }
.LBB0_359:
	s_lshl_b32 s18, s28, 11
	s_and_b32 s33, s18, 0x3f0000
	s_lshl_b32 s18, s28, 12
	s_and_b32 s31, s18, 0x7e0000
	s_ashr_i32 s18, s29, 7
	s_lshl_b32 s19, s29, 4
	s_and_b32 s30, s19, 0x7e0
	s_ashr_i32 s19, s18, 31
	s_lshl_b64 s[20:21], s[18:19], 23
	s_add_u32 s24, s92, s20
	v_readlane_b32 s26, v255, 0
	s_addc_u32 s25, s93, s21
	v_readlane_b32 s27, v255, 1
	s_lshl_b64 s[22:23], s[18:19], 22
	s_mov_b64 s[18:19], -1
	s_and_b64 vcc, exec, s[26:27]
	v_lshl_add_u64 v[134:135], v[110:111], 1, s[24:25]
	s_cbranch_vccz .LBB0_366
	global_load_dwordx4 v[0:3], v[112:113], off offset:16 nt
	global_load_dwordx4 v[4:7], v[112:113], off nt
	global_load_dwordx4 v[8:11], v[112:113], off offset:2064 nt
	global_load_dwordx4 v[12:15], v[112:113], off offset:2048 nt
	global_load_dwordx4 v[16:19], v[114:115], off offset:16 nt
	global_load_dwordx4 v[20:23], v[114:115], off nt
	s_cmp_eq_u32 s30, 0
	s_cbranch_scc1 .LBB0_362
	s_add_i32 s68, s30, -1
	s_lshl_b64 s[18:19], s[68:69], 12
	v_lshl_add_u64 v[28:29], v[134:135], 0, s[18:19]
	global_load_dwordx4 v[24:27], v[28:29], off offset:2048 nt
	s_nop 0
	global_load_dwordx4 v[28:31], v[28:29], off offset:3072 nt
	s_waitcnt vmcnt(0)
	v_lshlrev_b32_e32 v34, 16, v24
	v_and_b32_e32 v35, 0xffff0000, v24
	v_lshlrev_b32_e32 v36, 16, v28
	v_and_b32_e32 v37, 0xffff0000, v28
	v_lshlrev_b32_e32 v24, 16, v25
	v_and_b32_e32 v25, 0xffff0000, v25
	v_lshlrev_b32_e32 v28, 16, v29
	v_and_b32_e32 v29, 0xffff0000, v29
	v_lshlrev_b32_e32 v38, 16, v26
	v_and_b32_e32 v39, 0xffff0000, v26
	v_lshlrev_b32_e32 v40, 16, v30
	v_and_b32_e32 v41, 0xffff0000, v30
	v_lshlrev_b32_e32 v26, 16, v27
	v_and_b32_e32 v27, 0xffff0000, v27
	v_lshlrev_b32_e32 v30, 16, v31
	v_and_b32_e32 v31, 0xffff0000, v31
	v_pk_mul_f32 v[140:141], v[34:35], v[36:37]
	v_pk_mul_f32 v[142:143], v[24:25], v[28:29]
	v_pk_mul_f32 v[144:145], v[38:39], v[40:41]
	v_pk_mul_f32 v[146:147], v[26:27], v[30:31]
	s_branch .LBB0_363

; __device__ __forceinline__ void unpack8(const u32x4 w, float (&f)[8]) { f[0] = bf_lo(w.x); f[1] = bf_hi(w.x); f[2] = bf_lo(w.y); f[3] = bf_hi(w.y); f[4] = bf_lo(w.z); f[5] = bf_hi(w.z); f[6] = bf_lo(w.w); f[7] = bf_hi(w.w); }
; __device__ __forceinline__ u32x4 pack8(const float (&f)[8]) { u32x4 o; o.x = cvt_pk_bf16(f[0], f[1]); o.y = cvt_pk_bf16(f[2], f[3]); o.z = cvt_pk_bf16(f[4], f[5]); o.w = cvt_pk_bf16(f[6], f[7]); return o; }
; __global__ void __launch_bounds__(NWAVES * 64, 2) mk_fwd(Args args) {
;     ...
;                         { float c[8], v[8]; unpack8(*(const u32x4*)(pc + (size_t)t0 * EVEN_IN), c); unpack8(*(const u32x4*)(pv + (size_t)t0 * EVEN_IN), v);
; #pragma unroll
;                             for (int i = 0; i < 8; ++i) uc[i] = c[i] * v[i]; }
;                         for (int tc = t0; tc < t0 + 32; tc += 8) {
;                             u32x4 rc_[8], rv_[8], rg_[8];
; #pragma unroll
;                             for (int j = 0; j < 8; ++j) { const int t = tc + j, pn = (t + 1 < SEQ) ? t + 1 : SEQ - 1;
;                                 rc_[j] = *(const u32x4*)(pc + (size_t)pn * EVEN_IN); rv_[j] = *(const u32x4*)(pv + (size_t)pn * EVEN_IN); rg_[j] = *(const u32x4*)(pb + (size_t)t * EVEN_IN); }
;                             __builtin_amdgcn_sched_barrier(0);
; #pragma unroll
;                             for (int j = 0; j < 8; ++j) { const int t = tc + j; const float fn = (t + 1 < SEQ) ? 1.f : 0.f;
;                                 float c[8], v[8], bg[8], o[8]; unpack8(rc_[j], c); unpack8(rv_[j], v); unpack8(rg_[j], bg);
; #pragma unroll
;                                 for (int i = 0; i < 8; ++i) { un[i] = fn * (c[i] * v[i]); o[i] = bg[i] * (up[i] * w0[i] + uc[i] * w1[i] + un[i] * w2[i]); up[i] = uc[i]; uc[i] = un[i]; }
;                                 *(u32x4*)(cb + (size_t)t * D + 512 + ch0) = pack8(o); }
.LBB0_363:
	s_lshl_b32 s68, s30, 12
	v_lshl_add_u64 v[28:29], v[134:135], 0, s[68:69]
	global_load_dwordx4 v[24:27], v[28:29], off offset:2048 nt
	s_nop 0
	global_load_dwordx4 v[28:31], v[28:29], off offset:3072 nt
	s_mov_b64 s[18:19], 0x800
	v_lshl_add_u64 v[136:137], v[134:135], 0, s[18:19]
	s_mov_b64 s[18:19], 0xc00
	v_lshl_add_u64 v[138:139], v[134:135], 0, s[18:19]
	s_add_i32 s18, s30, 32
	s_add_u32 s19, s20, s31
	s_addc_u32 s25, s21, 0
	s_add_u32 s24, s84, s19
	s_addc_u32 s25, s85, s25
	s_add_u32 s19, s22, s33
	s_addc_u32 s27, s23, 0
	s_add_u32 s26, s84, s19
	s_addc_u32 s27, s85, s27
	s_mov_b32 s19, s30
	s_mov_b32 s40, 0x36004000
	s_mov_b32 s41, 0x36006000
	s_mov_b32 s46, 0x36007000
	s_mov_b32 s47, 0x3f001000
	s_mov_b32 s67, 0x3f002000
	s_mov_b32 s76, 0x3f003000
	s_waitcnt vmcnt(0)
	v_lshlrev_b32_e32 v34, 16, v24
	v_and_b32_e32 v35, 0xffff0000, v24
	v_lshlrev_b32_e32 v36, 16, v28
	v_and_b32_e32 v37, 0xffff0000, v28
	v_lshlrev_b32_e32 v24, 16, v25
	v_and_b32_e32 v25, 0xffff0000, v25
	v_lshlrev_b32_e32 v28, 16, v29
	v_and_b32_e32 v29, 0xffff0000, v29
	v_lshlrev_b32_e32 v38, 16, v26
	v_and_b32_e32 v39, 0xffff0000, v26
	v_lshlrev_b32_e32 v40, 16, v30
	v_and_b32_e32 v41, 0xffff0000, v30
	v_lshlrev_b32_e32 v26, 16, v27
	v_and_b32_e32 v27, 0xffff0000, v27
	v_lshlrev_b32_e32 v30, 16, v31
	v_and_b32_e32 v31, 0xffff0000, v31
	v_pk_mul_f32 v[148:149], v[34:35], v[36:37]
	v_pk_mul_f32 v[150:151], v[24:25], v[28:29]
	v_pk_mul_f32 v[152:153], v[38:39], v[40:41]
	v_pk_mul_f32 v[154:155], v[26:27], v[30:31]
.LBB0_364:
	s_nop 0
	v_lshl_add_u64 v[24:25], s[24:25], 0, v[132:133]
	v_add_co_u32_e32 v26, vcc, 0x36001000, v24
	s_mov_b32 s34, 0x36003000
	s_nop 0
	v_addc_co_u32_e32 v27, vcc, 0, v25, vcc
	v_add_co_u32_e32 v28, vcc, 0x36000000, v24
	s_nop 1
	v_addc_co_u32_e32 v29, vcc, 0, v25, vcc
	global_load_dwordx4 v[166:169], v[26:27], off offset:3072 nt
	global_load_dwordx4 v[170:173], v[28:29], off offset:1024 nt
	v_add_co_u32_e32 v28, vcc, 0x36002000, v24
	global_load_dwordx4 v[174:177], v[26:27], off offset:2048 nt
	global_load_dwordx4 v[98:101], v[26:27], off offset:1024 nt
	v_addc_co_u32_e32 v29, vcc, 0, v25, vcc
	v_add_co_u32_e32 v26, vcc, s34, v24
	s_mov_b32 s34, 0x36005000
	s_nop 0
	v_addc_co_u32_e32 v27, vcc, 0, v25, vcc
	v_add_co_u32_e32 v30, vcc, s40, v24
	global_load_dwordx4 v[94:97], v[26:27], off offset:2048 nt
	global_load_dwordx4 v[90:93], v[26:27], off offset:3072 nt
	global_load_dwordx4 v[102:105], v[28:29], off offset:2048 nt
	global_load_dwordx4 v[86:89], v[28:29], off offset:1024 nt
	v_addc_co_u32_e32 v31, vcc, 0, v25, vcc
	global_load_dwordx4 v[106:109], v[28:29], off offset:3072 nt
	global_load_dwordx4 v[74:77], v[26:27], off offset:1024 nt
	v_add_co_u32_e32 v26, vcc, s34, v24
	s_add_i32 s34, s19, 7
	s_nop 0
	v_addc_co_u32_e32 v27, vcc, 0, v25, vcc
	v_add_co_u32_e32 v58, vcc, s41, v24
	s_min_u32 s35, s34, 0x7fe
	s_nop 0
	v_addc_co_u32_e32 v59, vcc, 0, v25, vcc
	s_lshl_b32 s35, s35, 12
	v_add_co_u32_e32 v24, vcc, s46, v24
	s_add_i32 s68, s35, 0x1000
	global_load_dwordx4 v[70:73], v[26:27], off offset:2048 nt
	global_load_dwordx4 v[66:69], v[26:27], off offset:3072 nt
	global_load_dwordx4 v[78:81], v[30:31], off offset:2048 nt
	global_load_dwordx4 v[62:65], v[30:31], off offset:1024 nt
	global_load_dwordx4 v[82:85], v[30:31], off offset:3072 nt
	global_load_dwordx4 v[50:53], v[26:27], off offset:1024 nt
	v_addc_co_u32_e32 v25, vcc, 0, v25, vcc
	v_lshl_add_u64 v[26:27], v[136:137], 0, s[68:69]
	v_lshl_add_u64 v[28:29], v[138:139], 0, s[68:69]
	global_load_dwordx4 v[46:49], v[24:25], off offset:2048 nt
	global_load_dwordx4 v[42:45], v[24:25], off offset:3072 nt
	global_load_dwordx4 v[54:57], v[58:59], off offset:2048 nt
	global_load_dwordx4 v[38:41], v[58:59], off offset:1024 nt
	global_load_dwordx4 v[34:37], v[26:27], off nt
	s_nop 0
	global_load_dwordx4 v[28:31], v[28:29], off nt
	s_nop 0
	global_load_dwordx4 v[58:61], v[58:59], off offset:3072 nt
	s_nop 0
	global_load_dwordx4 v[24:27], v[24:25], off offset:1024 nt
	s_waitcnt vmcnt(21)
	v_lshlrev_b32_e32 v156, 16, v174
	v_and_b32_e32 v157, 0xffff0000, v174
	v_lshlrev_b32_e32 v158, 16, v166
	v_and_b32_e32 v159, 0xffff0000, v166
	v_pk_mul_f32 v[162:163], v[156:157], v[158:159]
	v_pk_mul_f32 v[156:157], v[148:149], v[12:13]
	v_lshlrev_b32_e32 v160, 16, v170
	v_pk_fma_f32 v[140:141], v[140:141], v[4:5], v[156:157]
	v_and_b32_e32 v161, 0xffff0000, v170
	v_pk_fma_f32 v[140:141], v[162:163], v[20:21], v[140:141]
	v_lshlrev_b32_e32 v158, 16, v167
	v_pk_mul_f32 v[156:157], v[140:141], v[160:161]
	v_lshlrev_b32_e32 v140, 16, v175
	v_and_b32_e32 v141, 0xffff0000, v175
	v_and_b32_e32 v159, 0xffff0000, v167
	v_pk_mul_f32 v[160:161], v[140:141], v[158:159]
	v_pk_mul_f32 v[140:141], v[150:151], v[14:15]
	v_lshlrev_b32_e32 v166, 16, v171
	v_pk_fma_f32 v[140:141], v[142:143], v[6:7], v[140:141]
	v_and_b32_e32 v167, 0xffff0000, v171
	v_pk_fma_f32 v[140:141], v[160:161], v[22:23], v[140:141]
	v_lshlrev_b32_e32 v142, 16, v168
	v_pk_mul_f32 v[166:167], v[140:141], v[166:167]
	v_lshlrev_b32_e32 v140, 16, v176
	v_and_b32_e32 v141, 0xffff0000, v176
	v_and_b32_e32 v143, 0xffff0000, v168
	v_pk_mul_f32 v[158:159], v[140:141], v[142:143]
	v_pk_mul_f32 v[140:141], v[152:153], v[8:9]
	v_lshlrev_b32_e32 v170, 16, v172
	v_pk_fma_f32 v[140:141], v[144:145], v[0:1], v[140:141]
	v_and_b32_e32 v171, 0xffff0000, v172
	v_pk_fma_f32 v[140:141], v[158:159], v[16:17], v[140:141]
	v_lshlrev_b32_e32 v142, 16, v169
	v_pk_mul_f32 v[144:145], v[140:141], v[170:171]
	v_lshlrev_b32_e32 v140, 16, v177
	v_and_b32_e32 v141, 0xffff0000, v177
	v_and_b32_e32 v143, 0xffff0000, v169
	v_pk_mul_f32 v[140:141], v[140:141], v[142:143]
	v_pk_mul_f32 v[142:143], v[154:155], v[10:11]
	v_lshlrev_b32_e32 v168, 16, v173
	v_pk_fma_f32 v[142:143], v[146:147], v[2:3], v[142:143]
	v_and_b32_e32 v169, 0xffff0000, v173
	v_pk_fma_f32 v[142:143], v[140:141], v[18:19], v[142:143]
	v_cvt_pk_bf16_f32 v144, v144, v145
	v_pk_mul_f32 v[146:147], v[142:143], v[168:169]
	v_cvt_pk_bf16_f32 v142, v156, v157
	v_lshl_add_u64 v[156:157], s[26:27], 0, v[132:133]
	v_cvt_pk_bf16_f32 v145, v146, v147
	v_add_co_u32_e32 v146, vcc, 0.5, v156
	v_cvt_pk_bf16_f32 v143, v166, v167
	s_nop 0
	v_addc_co_u32_e32 v147, vcc, 0, v157, vcc
	global_store_dwordx4 v[146:147], v[142:145], off offset:1024
	s_waitcnt vmcnt(21)
; __device__ __forceinline__ void unpack8(const u32x4 w, float (&f)[8]) { f[0] = bf_lo(w.x); f[1] = bf_hi(w.x); f[2] = bf_lo(w.y); f[3] = bf_hi(w.y); f[4] = bf_lo(w.z); f[5] = bf_hi(w.z); f[6] = bf_lo(w.w); f[7] = bf_hi(w.w); }
; __device__ __forceinline__ u32x4 pack8(const float (&f)[8]) { u32x4 o; o.x = cvt_pk_bf16(f[0], f[1]); o.y = cvt_pk_bf16(f[2], f[3]); o.z = cvt_pk_bf16(f[4], f[5]); o.w = cvt_pk_bf16(f[6], f[7]); return o; }
; __global__ void __launch_bounds__(NWAVES * 64, 2) mk_fwd(Args args) {
;     ...
;                         for (int tc = t0; tc < t0 + 32; tc += 8) {
;                             u32x4 rc_[8], rv_[8], rg_[8];
; #pragma unroll
;                             for (int j = 0; j < 8; ++j) { const int t = tc + j, pn = (t + 1 < SEQ) ? t + 1 : SEQ - 1;
;                                 rc_[j] = *(const u32x4*)(pc + (size_t)pn * EVEN_IN); rv_[j] = *(const u32x4*)(pv + (size_t)pn * EVEN_IN); rg_[j] = *(const u32x4*)(pb + (size_t)t * EVEN_IN); }
;                             __builtin_amdgcn_sched_barrier(0);
; #pragma unroll
;                             for (int j = 0; j < 8; ++j) { const int t = tc + j; const float fn = (t + 1 < SEQ) ? 1.f : 0.f;
;                                 float c[8], v[8], bg[8], o[8]; unpack8(rc_[j], c); unpack8(rv_[j], v); unpack8(rg_[j], bg);
; #pragma unroll
;                                 for (int i = 0; i < 8; ++i) { un[i] = fn * (c[i] * v[i]); o[i] = bg[i] * (up[i] * w0[i] + uc[i] * w1[i] + un[i] * w2[i]); up[i] = uc[i]; uc[i] = un[i]; }
;                                 *(u32x4*)(cb + (size_t)t * D + 512 + ch0) = pack8(o); }
	v_lshlrev_b32_e32 v166, 16, v98
	v_and_b32_e32 v167, 0xffff0000, v98
	s_waitcnt vmcnt(18)
	v_lshlrev_b32_e32 v142, 16, v102
	v_and_b32_e32 v143, 0xffff0000, v102
	s_waitcnt vmcnt(16)
	v_lshlrev_b32_e32 v144, 16, v106
	v_and_b32_e32 v145, 0xffff0000, v106
	v_pk_mul_f32 v[142:143], v[142:143], v[144:145]
	v_pk_mul_f32 v[144:145], v[162:163], v[12:13]
	v_lshlrev_b32_e32 v102, 16, v103
	v_and_b32_e32 v103, 0xffff0000, v103
	v_lshlrev_b32_e32 v106, 16, v107
	v_and_b32_e32 v107, 0xffff0000, v107
	v_pk_fma_f32 v[144:145], v[148:149], v[4:5], v[144:145]
	v_lshlrev_b32_e32 v148, 16, v99
	v_and_b32_e32 v149, 0xffff0000, v99
	v_pk_mul_f32 v[98:99], v[102:103], v[106:107]
	v_pk_mul_f32 v[102:103], v[160:161], v[14:15]
	v_pk_fma_f32 v[144:145], v[142:143], v[20:21], v[144:145]
	v_pk_fma_f32 v[102:103], v[150:151], v[6:7], v[102:103]
	v_lshlrev_b32_e32 v150, 16, v100
	v_pk_fma_f32 v[102:103], v[98:99], v[22:23], v[102:103]
	v_and_b32_e32 v151, 0xffff0000, v100
	v_pk_mul_f32 v[106:107], v[102:103], v[148:149]
	v_lshlrev_b32_e32 v102, 16, v104
	v_and_b32_e32 v103, 0xffff0000, v104
	v_lshlrev_b32_e32 v148, 16, v108
	v_and_b32_e32 v149, 0xffff0000, v108
	v_pk_mul_f32 v[102:103], v[102:103], v[148:149]
	v_pk_mul_f32 v[148:149], v[158:159], v[8:9]
	v_lshlrev_b32_e32 v104, 16, v105
	v_pk_fma_f32 v[148:149], v[152:153], v[0:1], v[148:149]
	v_and_b32_e32 v105, 0xffff0000, v105
	v_pk_fma_f32 v[148:149], v[102:103], v[16:17], v[148:149]
	v_lshlrev_b32_e32 v108, 16, v109
	v_and_b32_e32 v109, 0xffff0000, v109
	v_pk_mul_f32 v[148:149], v[148:149], v[150:151]
	v_lshlrev_b32_e32 v150, 16, v101
	v_and_b32_e32 v151, 0xffff0000, v101
	v_pk_mul_f32 v[100:101], v[104:105], v[108:109]
	v_pk_mul_f32 v[104:105], v[140:141], v[10:11]
	v_pk_mul_f32 v[144:145], v[144:145], v[166:167]
	v_pk_fma_f32 v[104:105], v[154:155], v[2:3], v[104:105]
	s_cmpk_lt_u32 s34, 0x7ff
	v_pk_fma_f32 v[104:105], v[100:101], v[18:19], v[104:105]
	s_cselect_b64 s[34:35], -1, 0
	v_pk_mul_f32 v[108:109], v[104:105], v[150:151]
	v_cvt_pk_bf16_f32 v104, v144, v145
	v_cvt_pk_bf16_f32 v105, v106, v107
	v_cvt_pk_bf16_f32 v106, v148, v149
	v_cvt_pk_bf16_f32 v107, v108, v109
	global_store_dwordx4 v[146:147], v[104:107], off offset:3072
	v_lshlrev_b32_e32 v108, 16, v86
	v_and_b32_e32 v109, 0xffff0000, v86
	v_lshlrev_b32_e32 v104, 16, v94
	v_and_b32_e32 v105, 0xffff0000, v94
	v_lshlrev_b32_e32 v106, 16, v90
	v_and_b32_e32 v107, 0xffff0000, v90
	v_pk_mul_f32 v[104:105], v[104:105], v[106:107]
	v_pk_mul_f32 v[106:107], v[142:143], v[12:13]
	v_lshlrev_b32_e32 v94, 16, v95
	v_pk_fma_f32 v[106:107], v[162:163], v[4:5], v[106:107]
	v_and_b32_e32 v95, 0xffff0000, v95
	v_pk_fma_f32 v[106:107], v[104:105], v[20:21], v[106:107]
	v_lshlrev_b32_e32 v90, 16, v91
	v_and_b32_e32 v91, 0xffff0000, v91
	v_pk_mul_f32 v[106:107], v[106:107], v[108:109]
	v_lshlrev_b32_e32 v108, 16, v87
	v_and_b32_e32 v109, 0xffff0000, v87
	v_pk_mul_f32 v[86:87], v[94:95], v[90:91]
	v_pk_mul_f32 v[90:91], v[98:99], v[14:15]
	v_lshlrev_b32_e32 v144, 16, v88
	v_pk_fma_f32 v[90:91], v[160:161], v[6:7], v[90:91]
	v_and_b32_e32 v145, 0xffff0000, v88
	v_pk_fma_f32 v[90:91], v[86:87], v[22:23], v[90:91]
	v_cndmask_b32_e64 v32, 0, 1.0, s[34:35]
	v_pk_mul_f32 v[94:95], v[90:91], v[108:109]
	v_lshlrev_b32_e32 v90, 16, v96
	v_and_b32_e32 v91, 0xffff0000, v96
	v_lshlrev_b32_e32 v108, 16, v92
	v_and_b32_e32 v109, 0xffff0000, v92
	v_pk_mul_f32 v[90:91], v[90:91], v[108:109]
	v_pk_mul_f32 v[108:109], v[102:103], v[8:9]
	v_lshlrev_b32_e32 v96, 16, v97
	v_pk_fma_f32 v[108:109], v[158:159], v[0:1], v[108:109]
	v_and_b32_e32 v97, 0xffff0000, v97
	v_pk_fma_f32 v[108:109], v[90:91], v[16:17], v[108:109]
	v_lshlrev_b32_e32 v92, 16, v93
	v_and_b32_e32 v93, 0xffff0000, v93
	v_pk_mul_f32 v[108:109], v[108:109], v[144:145]
	v_lshlrev_b32_e32 v144, 16, v89
	v_and_b32_e32 v145, 0xffff0000, v89
	v_pk_mul_f32 v[88:89], v[96:97], v[92:93]
	v_pk_mul_f32 v[92:93], v[100:101], v[10:11]
	s_add_i32 s19, s19, 8
	v_pk_fma_f32 v[92:93], v[140:141], v[2:3], v[92:93]
	s_add_u32 s24, s24, 0x8000
	v_pk_fma_f32 v[92:93], v[88:89], v[18:19], v[92:93]
	s_addc_u32 s25, s25, 0
	v_pk_mul_f32 v[96:97], v[92:93], v[144:145]
	v_cvt_pk_bf16_f32 v92, v106, v107
	v_add_co_u32_e32 v106, vcc, s47, v156
	v_cvt_pk_bf16_f32 v93, v94, v95
	v_cvt_pk_bf16_f32 v94, v108, v109
	v_cvt_pk_bf16_f32 v95, v96, v97
	v_addc_co_u32_e32 v107, vcc, 0, v157, vcc
	global_store_dwordx4 v[106:107], v[92:95], off offset:1024
	s_waitcnt vmcnt(17)
	v_lshlrev_b32_e32 v96, 16, v74
	v_and_b32_e32 v97, 0xffff0000, v74
	s_waitcnt vmcnt(14)
	v_lshlrev_b32_e32 v92, 16, v78
	v_and_b32_e32 v93, 0xffff0000, v78
	s_waitcnt vmcnt(12)
; __device__ __forceinline__ void unpack8(const u32x4 w, float (&f)[8]) { f[0] = bf_lo(w.x); f[1] = bf_hi(w.x); f[2] = bf_lo(w.y); f[3] = bf_hi(w.y); f[4] = bf_lo(w.z); f[5] = bf_hi(w.z); f[6] = bf_lo(w.w); f[7] = bf_hi(w.w); }
; __device__ __forceinline__ u32x4 pack8(const float (&f)[8]) { u32x4 o; o.x = cvt_pk_bf16(f[0], f[1]); o.y = cvt_pk_bf16(f[2], f[3]); o.z = cvt_pk_bf16(f[4], f[5]); o.w = cvt_pk_bf16(f[6], f[7]); return o; }
; __global__ void __launch_bounds__(NWAVES * 64, 2) mk_fwd(Args args) {
;     ...
;                         for (int tc = t0; tc < t0 + 32; tc += 8) {
;                             u32x4 rc_[8], rv_[8], rg_[8];
; #pragma unroll
;                             for (int j = 0; j < 8; ++j) { const int t = tc + j, pn = (t + 1 < SEQ) ? t + 1 : SEQ - 1;
;                                 rc_[j] = *(const u32x4*)(pc + (size_t)pn * EVEN_IN); rv_[j] = *(const u32x4*)(pv + (size_t)pn * EVEN_IN); rg_[j] = *(const u32x4*)(pb + (size_t)t * EVEN_IN); }
;                             __builtin_amdgcn_sched_barrier(0);
; #pragma unroll
;                             for (int j = 0; j < 8; ++j) { const int t = tc + j; const float fn = (t + 1 < SEQ) ? 1.f : 0.f;
;                                 float c[8], v[8], bg[8], o[8]; unpack8(rc_[j], c); unpack8(rv_[j], v); unpack8(rg_[j], bg);
; #pragma unroll
;                                 for (int i = 0; i < 8; ++i) { un[i] = fn * (c[i] * v[i]); o[i] = bg[i] * (up[i] * w0[i] + uc[i] * w1[i] + un[i] * w2[i]); up[i] = uc[i]; uc[i] = un[i]; }
;                                 *(u32x4*)(cb + (size_t)t * D + 512 + ch0) = pack8(o); }
	v_lshlrev_b32_e32 v94, 16, v82
	v_and_b32_e32 v95, 0xffff0000, v82
	v_lshlrev_b32_e32 v78, 16, v79
	v_and_b32_e32 v79, 0xffff0000, v79
	v_lshlrev_b32_e32 v82, 16, v83
	v_and_b32_e32 v83, 0xffff0000, v83
	v_pk_mul_f32 v[92:93], v[92:93], v[94:95]
	v_pk_mul_f32 v[94:95], v[104:105], v[12:13]
	v_pk_mul_f32 v[78:79], v[78:79], v[82:83]
	v_pk_mul_f32 v[82:83], v[86:87], v[14:15]
	v_pk_fma_f32 v[94:95], v[142:143], v[4:5], v[94:95]
	v_pk_fma_f32 v[82:83], v[98:99], v[6:7], v[82:83]
	v_pk_fma_f32 v[94:95], v[92:93], v[20:21], v[94:95]
	v_lshlrev_b32_e32 v74, 16, v75
	v_and_b32_e32 v75, 0xffff0000, v75
	v_pk_fma_f32 v[82:83], v[78:79], v[22:23], v[82:83]
	v_pk_mul_f32 v[94:95], v[94:95], v[96:97]
	v_pk_mul_f32 v[74:75], v[82:83], v[74:75]
	v_lshlrev_b32_e32 v82, 16, v80
	v_and_b32_e32 v83, 0xffff0000, v80
	v_lshlrev_b32_e32 v96, 16, v84
	v_and_b32_e32 v97, 0xffff0000, v84
	v_pk_mul_f32 v[82:83], v[82:83], v[96:97]
	v_pk_mul_f32 v[96:97], v[90:91], v[8:9]
	v_lshlrev_b32_e32 v98, 16, v76
	v_pk_fma_f32 v[96:97], v[102:103], v[0:1], v[96:97]
	v_and_b32_e32 v99, 0xffff0000, v76
	v_pk_fma_f32 v[96:97], v[82:83], v[16:17], v[96:97]
	v_lshlrev_b32_e32 v80, 16, v81
	v_and_b32_e32 v81, 0xffff0000, v81
	v_lshlrev_b32_e32 v84, 16, v85
	v_and_b32_e32 v85, 0xffff0000, v85
	v_pk_mul_f32 v[96:97], v[96:97], v[98:99]
	v_lshlrev_b32_e32 v98, 16, v77
	v_and_b32_e32 v99, 0xffff0000, v77
	v_pk_mul_f32 v[76:77], v[80:81], v[84:85]
	v_pk_mul_f32 v[80:81], v[88:89], v[10:11]
	v_cvt_pk_bf16_f32 v94, v94, v95
	v_pk_fma_f32 v[80:81], v[100:101], v[2:3], v[80:81]
	v_cvt_pk_bf16_f32 v95, v74, v75
	v_pk_fma_f32 v[80:81], v[76:77], v[18:19], v[80:81]
	v_cvt_pk_bf16_f32 v96, v96, v97
	v_pk_mul_f32 v[80:81], v[80:81], v[98:99]
	v_lshlrev_b32_e32 v74, 16, v70
	v_cvt_pk_bf16_f32 v97, v80, v81
	v_and_b32_e32 v75, 0xffff0000, v70
	v_lshlrev_b32_e32 v80, 16, v66
	v_and_b32_e32 v81, 0xffff0000, v66
	v_lshlrev_b32_e32 v70, 16, v71
	v_and_b32_e32 v71, 0xffff0000, v71
	v_lshlrev_b32_e32 v66, 16, v67
	v_and_b32_e32 v67, 0xffff0000, v67
	v_pk_mul_f32 v[74:75], v[74:75], v[80:81]
	v_pk_mul_f32 v[80:81], v[92:93], v[12:13]
	v_pk_mul_f32 v[66:67], v[70:71], v[66:67]
	v_pk_mul_f32 v[70:71], v[78:79], v[14:15]
	v_pk_fma_f32 v[80:81], v[104:105], v[4:5], v[80:81]
	v_pk_fma_f32 v[70:71], v[86:87], v[6:7], v[70:71]
	v_lshlrev_b32_e32 v84, 16, v62
	v_and_b32_e32 v85, 0xffff0000, v62
	v_pk_fma_f32 v[80:81], v[74:75], v[20:21], v[80:81]
	v_lshlrev_b32_e32 v62, 16, v63
	v_and_b32_e32 v63, 0xffff0000, v63
	v_pk_fma_f32 v[70:71], v[66:67], v[22:23], v[70:71]
	v_pk_mul_f32 v[80:81], v[80:81], v[84:85]
	v_pk_mul_f32 v[62:63], v[70:71], v[62:63]
	v_lshlrev_b32_e32 v70, 16, v72
	v_and_b32_e32 v71, 0xffff0000, v72
	v_lshlrev_b32_e32 v84, 16, v68
	v_and_b32_e32 v85, 0xffff0000, v68
	v_pk_mul_f32 v[70:71], v[70:71], v[84:85]
	v_pk_mul_f32 v[84:85], v[82:83], v[8:9]
	v_lshlrev_b32_e32 v86, 16, v64
	v_pk_fma_f32 v[84:85], v[90:91], v[0:1], v[84:85]
	v_and_b32_e32 v87, 0xffff0000, v64
	v_pk_fma_f32 v[84:85], v[70:71], v[16:17], v[84:85]
	v_lshlrev_b32_e32 v72, 16, v73
	v_and_b32_e32 v73, 0xffff0000, v73
	v_lshlrev_b32_e32 v68, 16, v69
	v_and_b32_e32 v69, 0xffff0000, v69
	v_pk_mul_f32 v[86:87], v[84:85], v[86:87]
	v_lshlrev_b32_e32 v84, 16, v65
	v_and_b32_e32 v85, 0xffff0000, v65
	v_pk_mul_f32 v[64:65], v[72:73], v[68:69]
	v_pk_mul_f32 v[68:69], v[76:77], v[10:11]
	s_waitcnt vmcnt(4)
	v_lshlrev_b32_e32 v72, 16, v58
	v_pk_fma_f32 v[68:69], v[88:89], v[2:3], v[68:69]
	v_and_b32_e32 v73, 0xffff0000, v58
	v_pk_fma_f32 v[68:69], v[64:65], v[18:19], v[68:69]
	v_lshlrev_b32_e32 v58, 16, v59
	v_pk_mul_f32 v[68:69], v[68:69], v[84:85]
	v_cvt_pk_bf16_f32 v85, v62, v63
	v_lshlrev_b32_e32 v62, 16, v54
	v_and_b32_e32 v63, 0xffff0000, v54
	v_lshlrev_b32_e32 v54, 16, v55
	v_and_b32_e32 v55, 0xffff0000, v55
	v_and_b32_e32 v59, 0xffff0000, v59
	v_pk_mul_f32 v[54:55], v[54:55], v[58:59]
	v_pk_mul_f32 v[58:59], v[66:67], v[14:15]
	v_cvt_pk_bf16_f32 v84, v80, v81
	v_pk_fma_f32 v[58:59], v[78:79], v[6:7], v[58:59]
	v_lshlrev_b32_e32 v80, 16, v50
	v_and_b32_e32 v81, 0xffff0000, v50
	v_lshlrev_b32_e32 v50, 16, v51
	v_and_b32_e32 v51, 0xffff0000, v51
	v_pk_fma_f32 v[58:59], v[54:55], v[22:23], v[58:59]
	v_pk_mul_f32 v[62:63], v[62:63], v[72:73]
	v_pk_mul_f32 v[72:73], v[74:75], v[12:13]
	v_pk_mul_f32 v[78:79], v[58:59], v[50:51]
	v_lshlrev_b32_e32 v50, 16, v56
	v_and_b32_e32 v51, 0xffff0000, v56
	v_lshlrev_b32_e32 v58, 16, v60
	v_and_b32_e32 v59, 0xffff0000, v60
	v_pk_fma_f32 v[72:73], v[92:93], v[4:5], v[72:73]
	v_pk_mul_f32 v[58:59], v[50:51], v[58:59]
	v_pk_mul_f32 v[50:51], v[70:71], v[8:9]
	v_pk_fma_f32 v[72:73], v[62:63], v[20:21], v[72:73]
	v_pk_fma_f32 v[50:51], v[82:83], v[0:1], v[50:51]
	v_pk_mul_f32 v[72:73], v[72:73], v[80:81]
	v_lshlrev_b32_e32 v80, 16, v52
	v_and_b32_e32 v81, 0xffff0000, v52
	v_pk_fma_f32 v[50:51], v[58:59], v[16:17], v[50:51]
	v_lshlrev_b32_e32 v56, 16, v61
	v_pk_mul_f32 v[80:81], v[50:51], v[80:81]
	v_lshlrev_b32_e32 v50, 16, v57
	v_and_b32_e32 v51, 0xffff0000, v57
	v_and_b32_e32 v57, 0xffff0000, v61
	v_pk_mul_f32 v[50:51], v[50:51], v[56:57]
	v_pk_mul_f32 v[56:57], v[64:65], v[10:11]
	v_lshlrev_b32_e32 v52, 16, v53
	v_pk_fma_f32 v[56:57], v[76:77], v[2:3], v[56:57]
	v_and_b32_e32 v53, 0xffff0000, v53
	v_pk_fma_f32 v[56:57], v[50:51], v[18:19], v[56:57]
	v_cvt_pk_bf16_f32 v77, v78, v79
	v_pk_mul_f32 v[52:53], v[56:57], v[52:53]
	v_lshlrev_b32_e32 v56, 16, v42
	v_cvt_pk_bf16_f32 v79, v52, v53
	v_lshlrev_b32_e32 v52, 16, v46
	v_and_b32_e32 v53, 0xffff0000, v46
	v_and_b32_e32 v57, 0xffff0000, v42
	v_lshlrev_b32_e32 v46, 16, v47
	v_and_b32_e32 v47, 0xffff0000, v47
	v_lshlrev_b32_e32 v42, 16, v43
; __device__ __forceinline__ void unpack8(const u32x4 w, float (&f)[8]) { f[0] = bf_lo(w.x); f[1] = bf_hi(w.x); f[2] = bf_lo(w.y); f[3] = bf_hi(w.y); f[4] = bf_lo(w.z); f[5] = bf_hi(w.z); f[6] = bf_lo(w.w); f[7] = bf_hi(w.w); }
; __device__ __forceinline__ u32x4 pack8(const float (&f)[8]) { u32x4 o; o.x = cvt_pk_bf16(f[0], f[1]); o.y = cvt_pk_bf16(f[2], f[3]); o.z = cvt_pk_bf16(f[4], f[5]); o.w = cvt_pk_bf16(f[6], f[7]); return o; }
; __global__ void __launch_bounds__(NWAVES * 64, 2) mk_fwd(Args args) {
;     ...
;                         for (int tc = t0; tc < t0 + 32; tc += 8) {
;                             u32x4 rc_[8], rv_[8], rg_[8];
; #pragma unroll
;                             for (int j = 0; j < 8; ++j) { const int t = tc + j, pn = (t + 1 < SEQ) ? t + 1 : SEQ - 1;
;                                 rc_[j] = *(const u32x4*)(pc + (size_t)pn * EVEN_IN); rv_[j] = *(const u32x4*)(pv + (size_t)pn * EVEN_IN); rg_[j] = *(const u32x4*)(pb + (size_t)t * EVEN_IN); }
;                             __builtin_amdgcn_sched_barrier(0);
; #pragma unroll
;                             for (int j = 0; j < 8; ++j) { const int t = tc + j; const float fn = (t + 1 < SEQ) ? 1.f : 0.f;
;                                 float c[8], v[8], bg[8], o[8]; unpack8(rc_[j], c); unpack8(rv_[j], v); unpack8(rg_[j], bg);
; #pragma unroll
;                                 for (int i = 0; i < 8; ++i) { un[i] = fn * (c[i] * v[i]); o[i] = bg[i] * (up[i] * w0[i] + uc[i] * w1[i] + un[i] * w2[i]); up[i] = uc[i]; uc[i] = un[i]; }
;                                 *(u32x4*)(cb + (size_t)t * D + 512 + ch0) = pack8(o); }
	v_and_b32_e32 v43, 0xffff0000, v43
	v_pk_mul_f32 v[142:143], v[46:47], v[42:43]
	v_pk_mul_f32 v[42:43], v[54:55], v[14:15]
	v_pk_mul_f32 v[140:141], v[52:53], v[56:57]
	v_pk_fma_f32 v[42:43], v[66:67], v[6:7], v[42:43]
	v_lshlrev_b32_e32 v52, 16, v38
	v_and_b32_e32 v53, 0xffff0000, v38
	v_lshlrev_b32_e32 v38, 16, v39
	v_and_b32_e32 v39, 0xffff0000, v39
	v_pk_fma_f32 v[42:43], v[142:143], v[22:23], v[42:43]
	v_lshlrev_b32_e32 v46, 16, v44
	v_pk_mul_f32 v[42:43], v[42:43], v[38:39]
	v_lshlrev_b32_e32 v38, 16, v48
	v_and_b32_e32 v39, 0xffff0000, v48
	v_and_b32_e32 v47, 0xffff0000, v44
	v_pk_mul_f32 v[144:145], v[38:39], v[46:47]
	v_pk_mul_f32 v[46:47], v[58:59], v[8:9]
	v_lshlrev_b32_e32 v38, 16, v40
	v_pk_fma_f32 v[46:47], v[70:71], v[0:1], v[46:47]
	v_and_b32_e32 v39, 0xffff0000, v40
	v_pk_fma_f32 v[46:47], v[144:145], v[16:17], v[46:47]
	v_lshlrev_b32_e32 v44, 16, v45
	v_pk_mul_f32 v[46:47], v[46:47], v[38:39]
	v_lshlrev_b32_e32 v38, 16, v49
	v_and_b32_e32 v39, 0xffff0000, v49
	v_and_b32_e32 v45, 0xffff0000, v45
	v_pk_mul_f32 v[56:57], v[62:63], v[12:13]
	v_pk_mul_f32 v[146:147], v[38:39], v[44:45]
	v_lshlrev_b32_e32 v38, 16, v41
	v_and_b32_e32 v39, 0xffff0000, v41
	v_pk_mul_f32 v[40:41], v[50:51], v[10:11]
	v_cvt_pk_bf16_f32 v86, v86, v87
	v_cvt_pk_bf16_f32 v87, v68, v69
	v_add_co_u32_e32 v68, vcc, s67, v156
	v_pk_fma_f32 v[56:57], v[74:75], v[4:5], v[56:57]
	v_pk_fma_f32 v[40:41], v[64:65], v[2:3], v[40:41]
	v_addc_co_u32_e32 v69, vcc, 0, v157, vcc
	v_pk_fma_f32 v[56:57], v[140:141], v[20:21], v[56:57]
	v_pk_fma_f32 v[40:41], v[146:147], v[18:19], v[40:41]
	v_pk_mul_f32 v[52:53], v[56:57], v[52:53]
	v_pk_mul_f32 v[44:45], v[40:41], v[38:39]
	v_cvt_pk_bf16_f32 v39, v42, v43
	v_add_co_u32_e32 v42, vcc, s76, v156
	v_cvt_pk_bf16_f32 v38, v52, v53
	v_cvt_pk_bf16_f32 v40, v46, v47
	v_cvt_pk_bf16_f32 v41, v44, v45
	v_addc_co_u32_e32 v43, vcc, 0, v157, vcc
	global_store_dwordx4 v[42:43], v[38:41], off offset:1024
	s_add_u32 s26, s26, 0x4000
	s_addc_u32 s27, s27, 0
	v_lshlrev_b32_e32 v38, 16, v34
	v_and_b32_e32 v39, 0xffff0000, v34
	v_lshlrev_b32_e32 v40, 16, v28
	v_and_b32_e32 v41, 0xffff0000, v28
	v_lshlrev_b32_e32 v34, 16, v35
	v_and_b32_e32 v35, 0xffff0000, v35
	v_lshlrev_b32_e32 v28, 16, v29
	v_and_b32_e32 v29, 0xffff0000, v29
	v_pk_mul_f32 v[28:29], v[34:35], v[28:29]
	v_pk_mul_f32 v[38:39], v[38:39], v[40:41]
	v_pk_mul_f32 v[150:151], v[32:33], v[28:29] op_sel_hi:[0,1]
	v_pk_mul_f32 v[28:29], v[142:143], v[14:15]
	v_pk_mul_f32 v[148:149], v[32:33], v[38:39] op_sel_hi:[0,1]
	v_pk_fma_f32 v[28:29], v[54:55], v[6:7], v[28:29]
	s_waitcnt vmcnt(4)
	v_lshlrev_b32_e32 v38, 16, v24
	v_and_b32_e32 v39, 0xffff0000, v24
	v_lshlrev_b32_e32 v24, 16, v25
	v_and_b32_e32 v25, 0xffff0000, v25
	v_pk_fma_f32 v[28:29], v[150:151], v[22:23], v[28:29]
	v_lshlrev_b32_e32 v34, 16, v30
	v_pk_mul_f32 v[28:29], v[28:29], v[24:25]
	v_lshlrev_b32_e32 v24, 16, v36
	v_and_b32_e32 v25, 0xffff0000, v36
	v_and_b32_e32 v35, 0xffff0000, v30
	v_pk_mul_f32 v[24:25], v[24:25], v[34:35]
	v_pk_mul_f32 v[34:35], v[144:145], v[8:9]
	v_pk_mul_f32 v[152:153], v[32:33], v[24:25] op_sel_hi:[0,1]
	v_pk_fma_f32 v[34:35], v[58:59], v[0:1], v[34:35]
	v_lshlrev_b32_e32 v24, 16, v26
	v_and_b32_e32 v25, 0xffff0000, v26
	v_pk_fma_f32 v[34:35], v[152:153], v[16:17], v[34:35]
	v_lshlrev_b32_e32 v30, 16, v31
	v_pk_mul_f32 v[34:35], v[34:35], v[24:25]
	v_lshlrev_b32_e32 v24, 16, v37
	v_and_b32_e32 v25, 0xffff0000, v37
	v_and_b32_e32 v31, 0xffff0000, v31
	v_pk_mul_f32 v[24:25], v[24:25], v[30:31]
	v_pk_mul_f32 v[40:41], v[140:141], v[12:13]
	v_pk_mul_f32 v[154:155], v[32:33], v[24:25] op_sel_hi:[0,1]
	v_lshlrev_b32_e32 v24, 16, v27
	v_and_b32_e32 v25, 0xffff0000, v27
	v_pk_mul_f32 v[26:27], v[146:147], v[10:11]
	v_pk_fma_f32 v[40:41], v[62:63], v[4:5], v[40:41]
	v_pk_fma_f32 v[26:27], v[50:51], v[2:3], v[26:27]
	v_pk_fma_f32 v[40:41], v[148:149], v[20:21], v[40:41]
	v_pk_fma_f32 v[26:27], v[154:155], v[18:19], v[26:27]
	v_pk_mul_f32 v[38:39], v[40:41], v[38:39]
	v_pk_mul_f32 v[30:31], v[26:27], v[24:25]
	v_cvt_pk_bf16_f32 v76, v72, v73
	v_cvt_pk_bf16_f32 v78, v80, v81
	v_cvt_pk_bf16_f32 v24, v38, v39
	v_cvt_pk_bf16_f32 v25, v28, v29
	v_cvt_pk_bf16_f32 v26, v34, v35
	v_cvt_pk_bf16_f32 v27, v30, v31
	s_cmp_lt_u32 s19, s18
	global_store_dwordx4 v[106:107], v[94:97], off offset:3072
	global_store_dwordx4 v[68:69], v[84:87], off offset:1024
	global_store_dwordx4 v[68:69], v[76:79], off offset:3072
	global_store_dwordx4 v[42:43], v[24:27], off offset:3072
	s_cbranch_scc1 .LBB0_364
	s_mov_b64 s[18:19], 0
	v_readlane_b32 s67, v254, 44
; __device__ __forceinline__ void unpack8(const u32x4 w, float (&f)[8]) { f[0] = bf_lo(w.x); f[1] = bf_hi(w.x); f[2] = bf_lo(w.y); f[3] = bf_hi(w.y); f[4] = bf_lo(w.z); f[5] = bf_hi(w.z); f[6] = bf_lo(w.w); f[7] = bf_hi(w.w); }
; __global__ void __launch_bounds__(NWAVES * 64, 2) mk_fwd(Args args) {
;     ...
;                     if (kind == 0) {
;                         const int ch0 = 8 * lane, half = 1 << (lane >> 4);
;                         const bf16_t* base = hb + ch0;
;                         float sum[8];
; #pragma unroll
;                         for (int i = 0; i < 8; ++i) sum[i] = 0.f;
;                         {   u32x4 r0[16];
; #pragma unroll
;                             for (int j = 0; j < 16; ++j) { int p = t0 + j - 8; p = p < 0 ? 0 : (p > SEQ - 1 ? SEQ - 1 : p); r0[j] = *(const u32x4*)(base + (size_t)p * EVEN_IN); }
;                             __builtin_amdgcn_sched_barrier(0);
; #pragma unroll
;                             for (int j = 0; j < 16; ++j) { const int dp = j - 8, p = t0 + dp; const float fl = (dp >= -half && dp < half && p >= 0 && p < SEQ) ? 1.f : 0.f;
;                                 float f[8]; unpack8(r0[j], f);
; #pragma unroll
;                                 for (int i = 0; i < 8; ++i) sum[i] += fl * f[i]; } }
.LBB0_366:
	s_and_b64 vcc, exec, s[18:19]
	s_cbranch_vccz .LBB0_358
	v_sub_u32_e64 v0, s30, 8 clamp
	s_or_b32 s18, s30, 1
	v_lshlrev_b32_e32 v32, 12, v0
	v_sub_u32_e64 v2, s18, 8 clamp
	v_lshl_add_u64 v[0:1], v[134:135], 0, v[32:33]
	v_lshlrev_b32_e32 v32, 12, v2
	s_or_b32 s18, s30, 2
	v_lshl_add_u64 v[2:3], v[134:135], 0, v[32:33]
	global_load_dwordx4 v[34:37], v[0:1], off nt
	global_load_dwordx4 v[38:41], v[2:3], off nt
	v_sub_u32_e64 v0, s18, 8 clamp
	s_or_b32 s18, s30, 3
	v_lshlrev_b32_e32 v32, 12, v0
	v_sub_u32_e64 v2, s18, 8 clamp
	v_lshl_add_u64 v[0:1], v[134:135], 0, v[32:33]
	v_lshlrev_b32_e32 v32, 12, v2
	s_or_b32 s18, s30, 4
	v_lshl_add_u64 v[2:3], v[134:135], 0, v[32:33]
	global_load_dwordx4 v[42:45], v[0:1], off nt
	global_load_dwordx4 v[46:49], v[2:3], off nt
	v_sub_u32_e64 v0, s18, 8 clamp
	s_or_b32 s18, s30, 5
	v_lshlrev_b32_e32 v32, 12, v0
	v_sub_u32_e64 v2, s18, 8 clamp
	v_lshl_add_u64 v[0:1], v[134:135], 0, v[32:33]
	v_lshlrev_b32_e32 v32, 12, v2
	s_or_b32 s18, s30, 6
	v_lshl_add_u64 v[2:3], v[134:135], 0, v[32:33]
	global_load_dwordx4 v[50:53], v[0:1], off nt
	global_load_dwordx4 v[54:57], v[2:3], off nt
	v_sub_u32_e64 v0, s18, 8 clamp
	s_or_b32 s18, s30, 7
	v_lshlrev_b32_e32 v32, 12, v0
	v_sub_u32_e64 v2, s18, 8 clamp
	s_lshl_b32 s68, s30, 12
	v_lshl_add_u64 v[0:1], v[134:135], 0, v[32:33]
	v_lshlrev_b32_e32 v32, 12, v2
	v_lshl_add_u64 v[4:5], v[134:135], 0, s[68:69]
	s_movk_i32 s18, 0x2000
	v_lshl_add_u64 v[2:3], v[134:135], 0, v[32:33]
	global_load_dwordx4 v[58:61], v[0:1], off nt
	global_load_dwordx4 v[62:65], v[2:3], off nt
	v_add_co_u32_e32 v0, vcc, s18, v4
	s_movk_i32 s18, 0x4000
	s_nop 0
	v_addc_co_u32_e32 v1, vcc, 0, v5, vcc
	global_load_dwordx4 v[24:27], v[0:1], off offset:-4096 nt
	global_load_dwordx4 v[16:19], v[0:1], off nt
	v_add_co_u32_e32 v0, vcc, s18, v4
	s_movk_i32 s18, 0x6000
	s_nop 0
	v_addc_co_u32_e32 v1, vcc, 0, v5, vcc
	global_load_dwordx4 v[20:23], v[0:1], off offset:-4096 nt
	global_load_dwordx4 v[8:11], v[0:1], off nt
	v_add_co_u32_e32 v0, vcc, s18, v4
	s_movk_i32 s18, 0x7000
	s_nop 0
	v_addc_co_u32_e32 v1, vcc, 0, v5, vcc
	v_add_co_u32_e32 v6, vcc, s18, v4
	global_load_dwordx4 v[12:15], v[0:1], off offset:-4096 nt
	s_nop 0
	global_load_dwordx4 v[0:3], v[0:1], off nt
	v_addc_co_u32_e32 v7, vcc, 0, v5, vcc
	global_load_dwordx4 v[66:69], v[4:5], off nt
	s_nop 0
	global_load_dwordx4 v[4:7], v[6:7], off nt
	s_cmp_lg_u32 s30, 0
	s_cselect_b64 s[18:19], -1, 0
	s_and_b64 s[18:19], s[4:5], s[18:19]
	v_cndmask_b32_e64 v28, 0, 1.0, s[18:19]
	v_cndmask_b32_e64 v30, v28, 0, s[2:3]
	s_waitcnt vmcnt(0)
	v_lshlrev_b32_e32 v76, 16, v34
	v_and_b32_e32 v77, 0xffff0000, v34
	v_lshlrev_b32_e32 v34, 16, v35
	v_and_b32_e32 v35, 0xffff0000, v35
	v_cndmask_b32_e64 v32, v28, 0, s[6:7]
	v_lshlrev_b32_e32 v78, 16, v38
	v_and_b32_e32 v79, 0xffff0000, v38
	v_pk_fma_f32 v[34:35], v[30:31], v[34:35], 0 op_sel_hi:[0,1,0]
	v_lshlrev_b32_e32 v38, 16, v39
	v_and_b32_e32 v39, 0xffff0000, v39
	v_cndmask_b32_e64 v70, v28, 0, s[8:9]
	v_pk_fma_f32 v[34:35], v[32:33], v[38:39], v[34:35] op_sel_hi:[0,1,1]
	v_lshlrev_b32_e32 v38, 16, v43
	v_and_b32_e32 v39, 0xffff0000, v43
	v_cndmask_b32_e64 v72, v28, 0, s[10:11]
	v_pk_fma_f32 v[34:35], v[70:71], v[38:39], v[34:35] op_sel_hi:[0,1,1]
	v_lshlrev_b32_e32 v38, 16, v47
	v_and_b32_e32 v39, 0xffff0000, v47
	v_cndmask_b32_e64 v74, v28, 0, s[12:13]
	v_pk_fma_f32 v[34:35], v[72:73], v[38:39], v[34:35] op_sel_hi:[0,1,1]
	v_lshlrev_b32_e32 v38, 16, v51
	v_and_b32_e32 v39, 0xffff0000, v51
	v_pk_fma_f32 v[34:35], v[74:75], v[38:39], v[34:35] op_sel_hi:[0,1,1]
	v_lshlrev_b32_e32 v38, 16, v36
	v_and_b32_e32 v39, 0xffff0000, v36
	v_lshlrev_b32_e32 v36, 16, v37
	v_and_b32_e32 v37, 0xffff0000, v37
	v_pk_fma_f32 v[76:77], v[30:31], v[76:77], 0 op_sel_hi:[0,1,0]
	v_pk_fma_f32 v[38:39], v[30:31], v[38:39], 0 op_sel_hi:[0,1,0]
	v_pk_fma_f32 v[30:31], v[30:31], v[36:37], 0 op_sel_hi:[0,1,0]
	v_lshlrev_b32_e32 v36, 16, v41
	v_and_b32_e32 v37, 0xffff0000, v41
	v_pk_fma_f32 v[76:77], v[32:33], v[78:79], v[76:77] op_sel_hi:[0,1,1]
	v_lshlrev_b32_e32 v78, 16, v42
	v_and_b32_e32 v79, 0xffff0000, v42
	v_pk_fma_f32 v[30:31], v[32:33], v[36:37], v[30:31] op_sel_hi:[0,1,1]
	v_lshlrev_b32_e32 v36, 16, v45
	v_and_b32_e32 v37, 0xffff0000, v45
	v_pk_fma_f32 v[76:77], v[70:71], v[78:79], v[76:77] op_sel_hi:[0,1,1]
	v_lshlrev_b32_e32 v78, 16, v46
	v_and_b32_e32 v79, 0xffff0000, v46
	v_lshlrev_b32_e32 v42, 16, v40
	v_and_b32_e32 v43, 0xffff0000, v40
	v_pk_fma_f32 v[30:31], v[70:71], v[36:37], v[30:31] op_sel_hi:[0,1,1]
	v_lshlrev_b32_e32 v36, 16, v49
	v_and_b32_e32 v37, 0xffff0000, v49
	v_pk_fma_f32 v[76:77], v[72:73], v[78:79], v[76:77] op_sel_hi:[0,1,1]
	v_lshlrev_b32_e32 v78, 16, v50
	v_and_b32_e32 v79, 0xffff0000, v50
	v_pk_fma_f32 v[38:39], v[32:33], v[42:43], v[38:39] op_sel_hi:[0,1,1]
	v_lshlrev_b32_e32 v42, 16, v44
	v_and_b32_e32 v43, 0xffff0000, v44
	v_pk_fma_f32 v[30:31], v[72:73], v[36:37], v[30:31] op_sel_hi:[0,1,1]
	v_lshlrev_b32_e32 v36, 16, v53
	v_and_b32_e32 v37, 0xffff0000, v53
	v_pk_fma_f32 v[76:77], v[74:75], v[78:79], v[76:77] op_sel_hi:[0,1,1]
	v_pk_fma_f32 v[38:39], v[70:71], v[42:43], v[38:39] op_sel_hi:[0,1,1]
	v_lshlrev_b32_e32 v42, 16, v48
	v_and_b32_e32 v43, 0xffff0000, v48
	v_pk_fma_f32 v[30:31], v[74:75], v[36:37], v[30:31] op_sel_hi:[0,1,1]
	v_cndmask_b32_e64 v32, v28, 0, s[14:15]
	v_lshlrev_b32_e32 v36, 16, v54
	v_and_b32_e32 v37, 0xffff0000, v54
	v_lshlrev_b32_e32 v40, 16, v55
	v_and_b32_e32 v41, 0xffff0000, v55
	v_pk_fma_f32 v[38:39], v[72:73], v[42:43], v[38:39] op_sel_hi:[0,1,1]
	v_lshlrev_b32_e32 v42, 16, v52
	v_and_b32_e32 v43, 0xffff0000, v52
	v_cndmask_b32_e64 v46, v28, 0, s[16:17]
; __device__ __forceinline__ void unpack8(const u32x4 w, float (&f)[8]) { f[0] = bf_lo(w.x); f[1] = bf_hi(w.x); f[2] = bf_lo(w.y); f[3] = bf_hi(w.y); f[4] = bf_lo(w.z); f[5] = bf_hi(w.z); f[6] = bf_lo(w.w); f[7] = bf_hi(w.w); }
; __global__ void __launch_bounds__(NWAVES * 64, 2) mk_fwd(Args args) {
;     ...
;                         {   u32x4 r0[16];
; #pragma unroll
;                             for (int j = 0; j < 16; ++j) { int p = t0 + j - 8; p = p < 0 ? 0 : (p > SEQ - 1 ? SEQ - 1 : p); r0[j] = *(const u32x4*)(base + (size_t)p * EVEN_IN); }
;                             __builtin_amdgcn_sched_barrier(0);
; #pragma unroll
;                             for (int j = 0; j < 16; ++j) { const int dp = j - 8, p = t0 + dp; const float fl = (dp >= -half && dp < half && p >= 0 && p < SEQ) ? 1.f : 0.f;
;                                 float f[8]; unpack8(r0[j], f);
; #pragma unroll
;                                 for (int i = 0; i < 8; ++i) sum[i] += fl * f[i]; } }
;                         for (int tc = t0; tc < t0 + 32; tc += 8) {
	v_lshlrev_b32_e32 v48, 16, v58
	v_and_b32_e32 v49, 0xffff0000, v58
	v_lshlrev_b32_e32 v50, 16, v59
	v_and_b32_e32 v51, 0xffff0000, v59
	v_pk_fma_f32 v[36:37], v[32:33], v[36:37], v[76:77] op_sel_hi:[0,1,1]
	v_pk_fma_f32 v[34:35], v[32:33], v[40:41], v[34:35] op_sel_hi:[0,1,1]
	v_pk_fma_f32 v[38:39], v[74:75], v[42:43], v[38:39] op_sel_hi:[0,1,1]
	v_lshlrev_b32_e32 v42, 16, v56
	v_and_b32_e32 v43, 0xffff0000, v56
	v_lshlrev_b32_e32 v44, 16, v57
	v_and_b32_e32 v45, 0xffff0000, v57
	v_lshlrev_b32_e32 v56, 16, v62
	v_and_b32_e32 v57, 0xffff0000, v62
	v_lshlrev_b32_e32 v58, 16, v63
	v_and_b32_e32 v59, 0xffff0000, v63
	v_pk_fma_f32 v[36:37], v[46:47], v[48:49], v[36:37] op_sel_hi:[0,1,1]
	v_pk_fma_f32 v[34:35], v[46:47], v[50:51], v[34:35] op_sel_hi:[0,1,1]
	v_lshlrev_b32_e32 v52, 16, v60
	v_and_b32_e32 v53, 0xffff0000, v60
	v_lshlrev_b32_e32 v54, 16, v61
	v_and_b32_e32 v55, 0xffff0000, v61
	v_lshlrev_b32_e32 v60, 16, v64
	v_and_b32_e32 v61, 0xffff0000, v64
	v_lshlrev_b32_e32 v62, 16, v65
	v_and_b32_e32 v63, 0xffff0000, v65
	v_lshlrev_b32_e32 v64, 16, v66
	v_and_b32_e32 v65, 0xffff0000, v66
	v_lshlrev_b32_e32 v66, 16, v67
	v_and_b32_e32 v67, 0xffff0000, v67
	v_pk_fma_f32 v[36:37], v[28:29], v[56:57], v[36:37] op_sel_hi:[0,1,1]
	v_pk_fma_f32 v[34:35], v[28:29], v[58:59], v[34:35] op_sel_hi:[0,1,1]
	v_pk_fma_f32 v[36:37], v[116:117], v[64:65], v[36:37]
	v_lshlrev_b32_e32 v48, 16, v24
	v_and_b32_e32 v49, 0xffff0000, v24
	v_pk_fma_f32 v[34:35], v[116:117], v[66:67], v[34:35]
	v_lshlrev_b32_e32 v24, 16, v25
	v_and_b32_e32 v25, 0xffff0000, v25
	v_pk_fma_f32 v[36:37], v[118:119], v[48:49], v[36:37]
	v_lshlrev_b32_e32 v48, 16, v16
	v_and_b32_e32 v49, 0xffff0000, v16
	v_pk_fma_f32 v[24:25], v[118:119], v[24:25], v[34:35]
	v_lshlrev_b32_e32 v16, 16, v17
	v_and_b32_e32 v17, 0xffff0000, v17
	v_pk_fma_f32 v[36:37], v[120:121], v[48:49], v[36:37]
	v_lshlrev_b32_e32 v48, 16, v20
	v_and_b32_e32 v49, 0xffff0000, v20
	v_pk_fma_f32 v[16:17], v[120:121], v[16:17], v[24:25]
	v_lshlrev_b32_e32 v20, 16, v21
	v_and_b32_e32 v21, 0xffff0000, v21
	v_pk_fma_f32 v[36:37], v[122:123], v[48:49], v[36:37]
	v_lshlrev_b32_e32 v48, 16, v8
	v_and_b32_e32 v49, 0xffff0000, v8
	v_pk_fma_f32 v[16:17], v[122:123], v[20:21], v[16:17]
	v_lshlrev_b32_e32 v8, 16, v9
	v_and_b32_e32 v9, 0xffff0000, v9
	v_pk_fma_f32 v[36:37], v[124:125], v[48:49], v[36:37]
	v_lshlrev_b32_e32 v48, 16, v12
	v_and_b32_e32 v49, 0xffff0000, v12
	v_pk_fma_f32 v[8:9], v[124:125], v[8:9], v[16:17]
	v_lshlrev_b32_e32 v12, 16, v13
	v_and_b32_e32 v13, 0xffff0000, v13
	v_pk_fma_f32 v[36:37], v[126:127], v[48:49], v[36:37]
	v_lshlrev_b32_e32 v48, 16, v0
	v_and_b32_e32 v49, 0xffff0000, v0
	v_pk_fma_f32 v[8:9], v[126:127], v[12:13], v[8:9]
	v_lshlrev_b32_e32 v0, 16, v1
	v_and_b32_e32 v1, 0xffff0000, v1
	v_pk_fma_f32 v[36:37], v[128:129], v[48:49], v[36:37]
	v_lshlrev_b32_e32 v48, 16, v4
	v_and_b32_e32 v49, 0xffff0000, v4
	v_pk_fma_f32 v[0:1], v[128:129], v[0:1], v[8:9]
	v_lshlrev_b32_e32 v4, 16, v5
	v_and_b32_e32 v5, 0xffff0000, v5
	v_pk_fma_f32 v[100:101], v[130:131], v[4:5], v[0:1]
	v_pk_fma_f32 v[0:1], v[32:33], v[42:43], v[38:39] op_sel_hi:[0,1,1]
	v_pk_fma_f32 v[0:1], v[46:47], v[52:53], v[0:1] op_sel_hi:[0,1,1]
	v_lshlrev_b32_e32 v70, 16, v68
	v_and_b32_e32 v71, 0xffff0000, v68
	v_pk_fma_f32 v[0:1], v[28:29], v[60:61], v[0:1] op_sel_hi:[0,1,1]
	v_pk_fma_f32 v[0:1], v[116:117], v[70:71], v[0:1]
	v_lshlrev_b32_e32 v4, 16, v26
	v_and_b32_e32 v5, 0xffff0000, v26
	v_pk_fma_f32 v[0:1], v[118:119], v[4:5], v[0:1]
	v_lshlrev_b32_e32 v4, 16, v18
	v_and_b32_e32 v5, 0xffff0000, v18
	v_pk_fma_f32 v[0:1], v[120:121], v[4:5], v[0:1]
	v_lshlrev_b32_e32 v4, 16, v22
	v_and_b32_e32 v5, 0xffff0000, v22
	v_pk_fma_f32 v[0:1], v[122:123], v[4:5], v[0:1]
	v_lshlrev_b32_e32 v4, 16, v10
	v_and_b32_e32 v5, 0xffff0000, v10
	v_pk_fma_f32 v[0:1], v[124:125], v[4:5], v[0:1]
	v_lshlrev_b32_e32 v4, 16, v14
	v_and_b32_e32 v5, 0xffff0000, v14
	v_pk_fma_f32 v[0:1], v[126:127], v[4:5], v[0:1]
	v_lshlrev_b32_e32 v4, 16, v2
	v_and_b32_e32 v5, 0xffff0000, v2
	v_pk_fma_f32 v[0:1], v[128:129], v[4:5], v[0:1]
	v_lshlrev_b32_e32 v4, 16, v6
	v_and_b32_e32 v5, 0xffff0000, v6
	v_pk_fma_f32 v[102:103], v[130:131], v[4:5], v[0:1]
	v_pk_fma_f32 v[0:1], v[32:33], v[44:45], v[30:31] op_sel_hi:[0,1,1]
	v_pk_fma_f32 v[0:1], v[46:47], v[54:55], v[0:1] op_sel_hi:[0,1,1]
	v_lshlrev_b32_e32 v68, 16, v69
	v_and_b32_e32 v69, 0xffff0000, v69
	v_pk_fma_f32 v[0:1], v[28:29], v[62:63], v[0:1] op_sel_hi:[0,1,1]
	s_add_i32 s18, s30, 32
	v_pk_fma_f32 v[0:1], v[116:117], v[68:69], v[0:1]
	v_lshlrev_b32_e32 v4, 16, v27
	v_and_b32_e32 v5, 0xffff0000, v27
	s_add_u32 s19, s22, s33
	v_pk_fma_f32 v[0:1], v[118:119], v[4:5], v[0:1]
	v_lshlrev_b32_e32 v4, 16, v19
	v_and_b32_e32 v5, 0xffff0000, v19
	s_addc_u32 s23, s23, 0
	v_pk_fma_f32 v[0:1], v[120:121], v[4:5], v[0:1]
	v_lshlrev_b32_e32 v4, 16, v23
	v_and_b32_e32 v5, 0xffff0000, v23
	s_add_u32 s22, s84, s19
	v_pk_fma_f32 v[0:1], v[122:123], v[4:5], v[0:1]
	v_lshlrev_b32_e32 v4, 16, v11
	v_and_b32_e32 v5, 0xffff0000, v11
	s_addc_u32 s23, s85, s23
	v_pk_fma_f32 v[0:1], v[124:125], v[4:5], v[0:1]
	v_lshlrev_b32_e32 v4, 16, v15
	v_and_b32_e32 v5, 0xffff0000, v15
	s_add_u32 s19, s20, s31
	v_pk_fma_f32 v[0:1], v[126:127], v[4:5], v[0:1]
	v_lshlrev_b32_e32 v2, 16, v3
	v_and_b32_e32 v3, 0xffff0000, v3
	s_addc_u32 s20, s21, 0
	v_pk_fma_f32 v[0:1], v[128:129], v[2:3], v[0:1]
	v_lshlrev_b32_e32 v2, 16, v7
	v_and_b32_e32 v3, 0xffff0000, v7
	s_add_u32 s24, s84, s19
	v_pk_fma_f32 v[98:99], v[130:131], v[48:49], v[36:37]
	v_pk_fma_f32 v[104:105], v[130:131], v[2:3], v[0:1]
	s_addc_u32 s25, s85, s20
	s_mov_b32 s26, 0x36004000
	s_mov_b32 s27, 0x36006000
	s_mov_b32 s31, 0x36007000
	s_mov_b32 s33, 0x3f001000
	s_mov_b32 s34, 0x3f002000
	s_mov_b32 s35, 0x3f003000
; __device__ __forceinline__ void unpack8(const u32x4 w, float (&f)[8]) { f[0] = bf_lo(w.x); f[1] = bf_hi(w.x); f[2] = bf_lo(w.y); f[3] = bf_hi(w.y); f[4] = bf_lo(w.z); f[5] = bf_hi(w.z); f[6] = bf_lo(w.w); f[7] = bf_hi(w.w); }
; __device__ __forceinline__ u32x4 pack8(const float (&f)[8]) { u32x4 o; o.x = cvt_pk_bf16(f[0], f[1]); o.y = cvt_pk_bf16(f[2], f[3]); o.z = cvt_pk_bf16(f[4], f[5]); o.w = cvt_pk_bf16(f[6], f[7]); return o; }
; __global__ void __launch_bounds__(NWAVES * 64, 2) mk_fwd(Args args) {
;     ...
;                         for (int tc = t0; tc < t0 + 32; tc += 8) {
;                             u32x4 ru[8], ra[8], rb[8];
; #pragma unroll
;                             for (int j = 0; j < 8; ++j) { const int t = tc + j, pa = (t + half < SEQ) ? t + half : SEQ - 1, pb = (t - half >= 0) ? t - half : 0;
;                                 ru[j] = *(const u32x4*)(base + (size_t)t * EVEN_IN); ra[j] = *(const u32x4*)(base + (size_t)pa * EVEN_IN); rb[j] = *(const u32x4*)(base + (size_t)pb * EVEN_IN); }
;                             __builtin_amdgcn_sched_barrier(0);
; #pragma unroll
;                             for (int j = 0; j < 8; ++j) { const int t = tc + j;
;                                 const int wlo = (t - half) > 0 ? (t - half) : 0, whi = (t + half) < SEQ ? (t + half) : SEQ;
;                                 const float rc = 1.0f / (float)(whi - wlo), fa = (t + half < SEQ) ? 1.f : 0.f, fb = (t - half >= 0) ? 1.f : 0.f;
;                                 float u[8], o[8], f[8]; unpack8(ru[j], u);
; #pragma unroll
;                                 for (int i = 0; i < 8; ++i) o[i] = sum[i] * rc - u[i];
;                                 *(u32x4*)(cb + (size_t)t * D + ch0) = pack8(o);
;                                 unpack8(ra[j], f);
; #pragma unroll
;                                 for (int i = 0; i < 8; ++i) sum[i] += fa * f[i];
;                                 unpack8(rb[j], f);
; #pragma unroll
;                                 for (int i = 0; i < 8; ++i) sum[i] -= fb * f[i]; }
.LBB0_368:
	v_add_u32_e32 v160, s30, v164
	v_min_i32_e32 v0, 0x7ff, v160
	v_lshl_add_u64 v[2:3], s[24:25], 0, v[132:133]
	v_add_u32_e32 v152, s30, v165
	v_add_co_u32_e32 v4, vcc, 0x36000000, v2
	v_ashrrev_i32_e32 v1, 31, v0
	v_max_i32_e32 v32, 0, v152
	v_addc_co_u32_e32 v5, vcc, 0, v3, vcc
	v_lshlrev_b64 v[0:1], 12, v[0:1]
	global_load_dwordx4 v[94:97], v[4:5], off nt
	v_lshl_add_u64 v[0:1], v[134:135], 0, v[0:1]
	v_lshlrev_b64 v[4:5], 12, v[32:33]
	v_add_u32_e32 v151, 1, v160
	v_lshl_add_u64 v[4:5], v[134:135], 0, v[4:5]
	global_load_dwordx4 v[86:89], v[0:1], off nt
	global_load_dwordx4 v[82:85], v[4:5], off nt
	v_min_i32_e32 v0, 0x7ff, v151
	v_add_u32_e32 v162, 1, v152
	v_ashrrev_i32_e32 v1, 31, v0
	v_max_i32_e32 v144, 0, v162
	v_lshlrev_b64 v[0:1], 12, v[0:1]
	v_mov_b32_e32 v145, v33
	v_lshl_add_u64 v[0:1], v[134:135], 0, v[0:1]
	v_lshlrev_b64 v[6:7], 12, v[144:145]
	v_add_u32_e32 v149, 2, v160
	s_mov_b32 s19, 0x36002000
	v_lshl_add_u64 v[6:7], v[134:135], 0, v[6:7]
	global_load_dwordx4 v[78:81], v[0:1], off nt
	global_load_dwordx4 v[74:77], v[6:7], off nt
	v_min_i32_e32 v0, 0x7ff, v149
	v_add_co_u32_e32 v4, vcc, s19, v2
	v_add_u32_e32 v150, 2, v152
	v_ashrrev_i32_e32 v1, 31, v0
	v_addc_co_u32_e32 v5, vcc, 0, v3, vcc
	v_max_i32_e32 v142, 0, v150
	v_lshlrev_b64 v[0:1], 12, v[0:1]
	v_mov_b32_e32 v143, v33
	global_load_dwordx4 v[90:93], v[4:5], off offset:-4096 nt
	global_load_dwordx4 v[70:73], v[4:5], off nt
	v_lshl_add_u64 v[0:1], v[134:135], 0, v[0:1]
	v_lshlrev_b64 v[4:5], 12, v[142:143]
	v_add_u32_e32 v145, 3, v160
	v_lshl_add_u64 v[4:5], v[134:135], 0, v[4:5]
	global_load_dwordx4 v[66:69], v[0:1], off nt
	global_load_dwordx4 v[62:65], v[4:5], off nt
	v_min_i32_e32 v0, 0x7ff, v145
	v_add_u32_e32 v148, 3, v152
	v_ashrrev_i32_e32 v1, 31, v0
	v_max_i32_e32 v140, 0, v148
	v_lshlrev_b64 v[0:1], 12, v[0:1]
	v_mov_b32_e32 v141, v33
	v_lshl_add_u64 v[0:1], v[134:135], 0, v[0:1]
	v_lshlrev_b64 v[6:7], 12, v[140:141]
	v_add_u32_e32 v146, 4, v160
	v_lshl_add_u64 v[6:7], v[134:135], 0, v[6:7]
	global_load_dwordx4 v[58:61], v[0:1], off nt
	global_load_dwordx4 v[54:57], v[6:7], off nt
	v_min_i32_e32 v0, 0x7ff, v146
	v_add_co_u32_e32 v4, vcc, s26, v2
	v_add_u32_e32 v147, 4, v152
	v_ashrrev_i32_e32 v1, 31, v0
	v_addc_co_u32_e32 v5, vcc, 0, v3, vcc
	v_max_i32_e32 v138, 0, v147
	v_lshlrev_b64 v[0:1], 12, v[0:1]
	v_mov_b32_e32 v139, v33
	global_load_dwordx4 v[46:49], v[4:5], off offset:-4096 nt
	global_load_dwordx4 v[42:45], v[4:5], off nt
	v_lshl_add_u64 v[0:1], v[134:135], 0, v[0:1]
	v_lshlrev_b64 v[4:5], 12, v[138:139]
	v_add_u32_e32 v156, 5, v160
	v_lshl_add_u64 v[4:5], v[134:135], 0, v[4:5]
	global_load_dwordx4 v[50:53], v[0:1], off nt
	global_load_dwordx4 v[34:37], v[4:5], off nt
	v_min_i32_e32 v0, 0x7ff, v156
	v_add_u32_e32 v158, 5, v152
	v_ashrrev_i32_e32 v1, 31, v0
	v_max_i32_e32 v106, 0, v158
	v_lshlrev_b64 v[0:1], 12, v[0:1]
	v_mov_b32_e32 v107, v33
	v_lshl_add_u64 v[0:1], v[134:135], 0, v[0:1]
	v_lshlrev_b64 v[6:7], 12, v[106:107]
	v_add_u32_e32 v157, 6, v160
	v_lshl_add_u64 v[6:7], v[134:135], 0, v[6:7]
	global_load_dwordx4 v[28:31], v[0:1], off nt
	global_load_dwordx4 v[24:27], v[6:7], off nt
	v_min_i32_e32 v0, 0x7ff, v157
	v_add_co_u32_e32 v4, vcc, s27, v2
	v_add_u32_e32 v159, 6, v152
	v_ashrrev_i32_e32 v1, 31, v0
	v_addc_co_u32_e32 v5, vcc, 0, v3, vcc
	v_max_i32_e32 v136, 0, v159
	v_lshlrev_b64 v[0:1], 12, v[0:1]
	v_mov_b32_e32 v137, v33
	global_load_dwordx4 v[38:41], v[4:5], off offset:-4096 nt
	global_load_dwordx4 v[20:23], v[4:5], off nt
	v_lshl_add_u64 v[0:1], v[134:135], 0, v[0:1]
	v_lshlrev_b64 v[4:5], 12, v[136:137]
	v_add_u32_e32 v107, 7, v160
	v_lshl_add_u64 v[4:5], v[134:135], 0, v[4:5]
	global_load_dwordx4 v[16:19], v[0:1], off nt
	global_load_dwordx4 v[12:15], v[4:5], off nt
	v_min_i32_e32 v0, 0x7ff, v107
	v_add_u32_e32 v137, 7, v152
	v_add_co_u32_e32 v2, vcc, s31, v2
	v_max_i32_e32 v108, 0, v137
	s_nop 0
	v_addc_co_u32_e32 v3, vcc, 0, v3, vcc
	v_ashrrev_i32_e32 v1, 31, v0
	v_mov_b32_e32 v109, v33
	global_load_dwordx4 v[8:11], v[2:3], off nt
	v_lshlrev_b64 v[0:1], 12, v[0:1]
	v_lshlrev_b64 v[2:3], 12, v[108:109]
	v_lshl_add_u64 v[0:1], v[134:135], 0, v[0:1]
	v_lshl_add_u64 v[2:3], v[134:135], 0, v[2:3]
	global_load_dwordx4 v[4:7], v[0:1], off nt
	s_nop 0
	global_load_dwordx4 v[0:3], v[2:3], off nt
	v_min_i32_e32 v109, 0x800, v160
	v_sub_u32_e32 v32, v109, v32
	v_cvt_f32_i32_e32 v32, v32
	s_waitcnt vmcnt(23)
	v_lshlrev_b32_e32 v154, 16, v96
	v_and_b32_e32 v155, 0xffff0000, v96
	v_lshlrev_b32_e32 v96, 16, v97
	v_div_scale_f32 v109, s[20:21], v32, v32, 1.0
	v_rcp_f32_e32 v139, v109
	v_and_b32_e32 v97, 0xffff0000, v97
	v_cmp_gt_i32_e64 s[20:21], s39, v160
	s_add_i32 s30, s30, 8
	v_fma_f32 v141, -v109, v139, 1.0
	v_fmac_f32_e32 v139, v141, v139
	v_div_scale_f32 v141, vcc, 1.0, v32, 1.0
	v_mul_f32_e32 v143, v141, v139
	v_fma_f32 v153, -v109, v143, v141
	v_fmac_f32_e32 v143, v153, v139
	v_fma_f32 v109, -v109, v143, v141
	v_div_fmas_f32 v109, v109, v139, v143
	v_div_fixup_f32 v32, v109, v32, 1.0
	v_cmp_lt_i32_e32 vcc, -1, v152
	v_lshlrev_b32_e32 v152, 16, v94
	v_and_b32_e32 v153, 0xffff0000, v94
	v_lshlrev_b32_e32 v94, 16, v95
	v_and_b32_e32 v95, 0xffff0000, v95
	v_min_i32_e32 v109, 0x800, v151
	v_pk_fma_f32 v[152:153], v[32:33], v[98:99], v[152:153] op_sel_hi:[0,1,1] neg_lo:[0,0,1] neg_hi:[0,0,1]
	v_pk_fma_f32 v[94:95], v[32:33], v[100:101], v[94:95] op_sel_hi:[0,1,1] neg_lo:[0,0,1] neg_hi:[0,0,1]
	v_sub_u32_e32 v109, v109, v144
	v_cvt_pk_bf16_f32 v152, v152, v153
	v_cvt_pk_bf16_f32 v153, v94, v95
	v_lshl_add_u64 v[94:95], s[22:23], 0, v[132:133]
	v_cvt_f32_i32_e32 v109, v109
	v_pk_fma_f32 v[154:155], v[32:33], v[102:103], v[154:155] op_sel_hi:[0,1,1] neg_lo:[0,0,1] neg_hi:[0,0,1]
	v_pk_fma_f32 v[96:97], v[32:33], v[104:105], v[96:97] op_sel_hi:[0,1,1] neg_lo:[0,0,1] neg_hi:[0,0,1]
	v_cndmask_b32_e64 v32, 0, 1.0, s[20:21]
	v_add_co_u32_e64 v160, s[20:21], 0.5, v94
	v_cvt_pk_bf16_f32 v154, v154, v155
	s_nop 0
	v_addc_co_u32_e64 v161, s[20:21], 0, v95, s[20:21]
	v_cvt_pk_bf16_f32 v155, v96, v97
	v_add_co_u32_e64 v96, s[20:21], s33, v94
	s_add_u32 s22, s22, 0x4000
	s_nop 0
	v_addc_co_u32_e64 v97, s[20:21], 0, v95, s[20:21]
	v_div_scale_f32 v139, s[20:21], v109, v109, 1.0
	v_rcp_f32_e32 v141, v139
	global_store_dwordx4 v[96:97], v[152:155], off offset:-4096
	v_cmp_gt_i32_e64 s[20:21], s39, v151
	s_waitcnt vmcnt(11)
; __device__ __forceinline__ void unpack8(const u32x4 w, float (&f)[8]) { f[0] = bf_lo(w.x); f[1] = bf_hi(w.x); f[2] = bf_lo(w.y); f[3] = bf_hi(w.y); f[4] = bf_lo(w.z); f[5] = bf_hi(w.z); f[6] = bf_lo(w.w); f[7] = bf_hi(w.w); }
; __device__ __forceinline__ u32x4 pack8(const float (&f)[8]) { u32x4 o; o.x = cvt_pk_bf16(f[0], f[1]); o.y = cvt_pk_bf16(f[2], f[3]); o.z = cvt_pk_bf16(f[4], f[5]); o.w = cvt_pk_bf16(f[6], f[7]); return o; }
; __global__ void __launch_bounds__(NWAVES * 64, 2) mk_fwd(Args args) {
;     ...
;                             for (int j = 0; j < 8; ++j) { const int t = tc + j;
;                                 const int wlo = (t - half) > 0 ? (t - half) : 0, whi = (t + half) < SEQ ? (t + half) : SEQ;
;                                 const float rc = 1.0f / (float)(whi - wlo), fa = (t + half < SEQ) ? 1.f : 0.f, fb = (t - half >= 0) ? 1.f : 0.f;
;                                 float u[8], o[8], f[8]; unpack8(ru[j], u);
; #pragma unroll
;                                 for (int i = 0; i < 8; ++i) o[i] = sum[i] * rc - u[i];
;                                 *(u32x4*)(cb + (size_t)t * D + ch0) = pack8(o);
;                                 unpack8(ra[j], f);
; #pragma unroll
;                                 for (int i = 0; i < 8; ++i) sum[i] += fa * f[i];
;                                 unpack8(rb[j], f);
; #pragma unroll
;                                 for (int i = 0; i < 8; ++i) sum[i] -= fb * f[i]; }
	v_and_b32_e32 v151, 0xffff0000, v50
	v_fma_f32 v143, -v139, v141, 1.0
	v_cndmask_b32_e64 v152, 0, 1.0, vcc
	v_fmac_f32_e32 v141, v143, v141
	v_div_scale_f32 v143, vcc, 1.0, v109, 1.0
	v_mul_f32_e32 v144, v143, v141
	v_fma_f32 v153, -v139, v144, v143
	v_fmac_f32_e32 v144, v153, v141
	v_fma_f32 v139, -v139, v144, v143
	v_lshlrev_b32_e32 v154, 16, v86
	v_and_b32_e32 v155, 0xffff0000, v86
	v_lshlrev_b32_e32 v86, 16, v87
	v_and_b32_e32 v87, 0xffff0000, v87
	v_div_fmas_f32 v139, v139, v141, v144
	v_pk_fma_f32 v[98:99], v[32:33], v[154:155], v[98:99] op_sel_hi:[0,1,1]
	v_lshlrev_b32_e32 v154, 16, v82
	v_and_b32_e32 v155, 0xffff0000, v82
	v_pk_fma_f32 v[86:87], v[32:33], v[86:87], v[100:101] op_sel_hi:[0,1,1]
	v_lshlrev_b32_e32 v82, 16, v83
	v_and_b32_e32 v83, 0xffff0000, v83
	v_div_fixup_f32 v144, v139, v109, 1.0
	v_pk_fma_f32 v[86:87], v[152:153], v[82:83], v[86:87] op_sel_hi:[0,1,1] neg_lo:[1,0,0] neg_hi:[1,0,0]
	v_lshlrev_b32_e32 v82, 16, v91
	v_and_b32_e32 v83, 0xffff0000, v91
	v_pk_fma_f32 v[98:99], v[152:153], v[154:155], v[98:99] op_sel_hi:[0,1,1] neg_lo:[1,0,0] neg_hi:[1,0,0]
	v_lshlrev_b32_e32 v154, 16, v90
	v_and_b32_e32 v155, 0xffff0000, v90
	v_pk_fma_f32 v[90:91], v[144:145], v[86:87], v[82:83] op_sel_hi:[0,1,1] neg_lo:[0,0,1] neg_hi:[0,0,1]
	v_lshlrev_b32_e32 v82, 16, v88
	v_and_b32_e32 v83, 0xffff0000, v88
	v_pk_fma_f32 v[82:83], v[32:33], v[82:83], v[102:103] op_sel_hi:[0,1,1]
	v_lshlrev_b32_e32 v100, 16, v84
	v_and_b32_e32 v101, 0xffff0000, v84
	v_pk_fma_f32 v[100:101], v[152:153], v[100:101], v[82:83] op_sel_hi:[0,1,1] neg_lo:[1,0,0] neg_hi:[1,0,0]
	v_lshlrev_b32_e32 v82, 16, v92
	v_and_b32_e32 v83, 0xffff0000, v92
	v_pk_fma_f32 v[102:103], v[144:145], v[100:101], v[82:83] op_sel_hi:[0,1,1] neg_lo:[0,0,1] neg_hi:[0,0,1]
	v_lshlrev_b32_e32 v82, 16, v89
	v_and_b32_e32 v83, 0xffff0000, v89
	v_pk_fma_f32 v[82:83], v[32:33], v[82:83], v[104:105] op_sel_hi:[0,1,1]
	v_lshlrev_b32_e32 v84, 16, v85
	v_and_b32_e32 v85, 0xffff0000, v85
	v_pk_fma_f32 v[88:89], v[152:153], v[84:85], v[82:83] op_sel_hi:[0,1,1] neg_lo:[1,0,0] neg_hi:[1,0,0]
	v_lshlrev_b32_e32 v82, 16, v93
	v_and_b32_e32 v83, 0xffff0000, v93
	v_pk_fma_f32 v[154:155], v[144:145], v[98:99], v[154:155] op_sel_hi:[0,1,1] neg_lo:[0,0,1] neg_hi:[0,0,1]
	v_pk_fma_f32 v[92:93], v[144:145], v[88:89], v[82:83] op_sel_hi:[0,1,1] neg_lo:[0,0,1] neg_hi:[0,0,1]
	v_cvt_pk_bf16_f32 v82, v154, v155
	v_cvt_pk_bf16_f32 v83, v90, v91
	v_cvt_pk_bf16_f32 v84, v102, v103
	v_cvt_pk_bf16_f32 v85, v92, v93
	global_store_dwordx4 v[160:161], v[82:85], off offset:2048
	v_cndmask_b32_e64 v32, 0, 1.0, s[20:21]
	v_cmp_lt_i32_e32 vcc, -1, v162
	v_min_i32_e32 v83, 0x800, v149
	v_sub_u32_e32 v83, v83, v142
	v_cvt_f32_i32_e32 v83, v83
	v_cndmask_b32_e64 v82, 0, 1.0, vcc
	v_and_b32_e32 v93, 0xffff0000, v74
	v_lshlrev_b32_e32 v154, 16, v62
	v_div_scale_f32 v84, s[20:21], v83, v83, 1.0
	v_rcp_f32_e32 v85, v84
	v_cmp_gt_i32_e64 s[20:21], s39, v149
	v_and_b32_e32 v155, 0xffff0000, v62
	v_lshlrev_b32_e32 v142, 16, v63
	v_fma_f32 v90, -v84, v85, 1.0
	v_fmac_f32_e32 v85, v90, v85
	v_div_scale_f32 v90, vcc, 1.0, v83, 1.0
	v_mul_f32_e32 v91, v90, v85
	v_fma_f32 v92, -v84, v91, v90
	v_fmac_f32_e32 v91, v92, v85
	v_fma_f32 v84, -v84, v91, v90
	v_div_fmas_f32 v84, v84, v85, v91
	v_lshlrev_b32_e32 v90, 16, v78
	v_and_b32_e32 v91, 0xffff0000, v78
	v_lshlrev_b32_e32 v78, 16, v79
	v_and_b32_e32 v79, 0xffff0000, v79
	v_pk_fma_f32 v[90:91], v[32:33], v[90:91], v[98:99] op_sel_hi:[0,1,1]
	v_lshlrev_b32_e32 v92, 16, v74
	v_pk_fma_f32 v[78:79], v[32:33], v[78:79], v[86:87] op_sel_hi:[0,1,1]
	v_lshlrev_b32_e32 v74, 16, v75
	v_and_b32_e32 v75, 0xffff0000, v75
	v_div_fixup_f32 v84, v84, v83, 1.0
	v_pk_fma_f32 v[90:91], v[82:83], v[92:93], v[90:91] op_sel_hi:[0,1,1] neg_lo:[1,0,0] neg_hi:[1,0,0]
	v_lshlrev_b32_e32 v92, 16, v70
	v_and_b32_e32 v93, 0xffff0000, v70
	v_pk_fma_f32 v[74:75], v[82:83], v[74:75], v[78:79] op_sel_hi:[0,1,1] neg_lo:[1,0,0] neg_hi:[1,0,0]
	v_lshlrev_b32_e32 v70, 16, v71
	v_and_b32_e32 v71, 0xffff0000, v71
	v_pk_fma_f32 v[78:79], v[84:85], v[74:75], v[70:71] op_sel_hi:[0,1,1] neg_lo:[0,0,1] neg_hi:[0,0,1]
	v_lshlrev_b32_e32 v70, 16, v80
	v_and_b32_e32 v71, 0xffff0000, v80
	v_pk_fma_f32 v[70:71], v[32:33], v[70:71], v[100:101] op_sel_hi:[0,1,1]
	v_lshlrev_b32_e32 v86, 16, v76
	v_and_b32_e32 v87, 0xffff0000, v76
	v_pk_fma_f32 v[86:87], v[82:83], v[86:87], v[70:71] op_sel_hi:[0,1,1] neg_lo:[1,0,0] neg_hi:[1,0,0]
	v_lshlrev_b32_e32 v70, 16, v72
	v_and_b32_e32 v71, 0xffff0000, v72
	v_pk_fma_f32 v[98:99], v[84:85], v[86:87], v[70:71] op_sel_hi:[0,1,1] neg_lo:[0,0,1] neg_hi:[0,0,1]
	v_lshlrev_b32_e32 v70, 16, v81
	v_and_b32_e32 v71, 0xffff0000, v81
	v_pk_fma_f32 v[70:71], v[32:33], v[70:71], v[88:89] op_sel_hi:[0,1,1]
	v_lshlrev_b32_e32 v76, 16, v77
	v_and_b32_e32 v77, 0xffff0000, v77
	v_pk_fma_f32 v[76:77], v[82:83], v[76:77], v[70:71] op_sel_hi:[0,1,1] neg_lo:[1,0,0] neg_hi:[1,0,0]
	v_lshlrev_b32_e32 v70, 16, v73
	v_and_b32_e32 v71, 0xffff0000, v73
	v_pk_fma_f32 v[92:93], v[84:85], v[90:91], v[92:93] op_sel_hi:[0,1,1] neg_lo:[0,0,1] neg_hi:[0,0,1]
	v_pk_fma_f32 v[80:81], v[84:85], v[76:77], v[70:71] op_sel_hi:[0,1,1] neg_lo:[0,0,1] neg_hi:[0,0,1]
	v_cvt_pk_bf16_f32 v70, v92, v93
	v_cvt_pk_bf16_f32 v71, v78, v79
	v_cvt_pk_bf16_f32 v72, v98, v99
	v_cvt_pk_bf16_f32 v73, v80, v81
	v_cndmask_b32_e64 v32, 0, 1.0, s[20:21]
	global_store_dwordx4 v[96:97], v[70:73], off
	v_and_b32_e32 v143, 0xffff0000, v63
	v_cmp_lt_i32_e32 vcc, -1, v150
	v_lshlrev_b32_e32 v70, 16, v66
	v_and_b32_e32 v71, 0xffff0000, v66
	v_lshlrev_b32_e32 v66, 16, v67
	v_and_b32_e32 v67, 0xffff0000, v67
	v_pk_fma_f32 v[100:101], v[32:33], v[66:67], v[74:75] op_sel_hi:[0,1,1]
; __device__ __forceinline__ void unpack8(const u32x4 w, float (&f)[8]) { f[0] = bf_lo(w.x); f[1] = bf_hi(w.x); f[2] = bf_lo(w.y); f[3] = bf_hi(w.y); f[4] = bf_lo(w.z); f[5] = bf_hi(w.z); f[6] = bf_lo(w.w); f[7] = bf_hi(w.w); }
; __device__ __forceinline__ u32x4 pack8(const float (&f)[8]) { u32x4 o; o.x = cvt_pk_bf16(f[0], f[1]); o.y = cvt_pk_bf16(f[2], f[3]); o.z = cvt_pk_bf16(f[4], f[5]); o.w = cvt_pk_bf16(f[6], f[7]); return o; }
; __global__ void __launch_bounds__(NWAVES * 64, 2) mk_fwd(Args args) {
;     ...
;                             for (int j = 0; j < 8; ++j) { const int t = tc + j;
;                                 const int wlo = (t - half) > 0 ? (t - half) : 0, whi = (t + half) < SEQ ? (t + half) : SEQ;
;                                 const float rc = 1.0f / (float)(whi - wlo), fa = (t + half < SEQ) ? 1.f : 0.f, fb = (t - half >= 0) ? 1.f : 0.f;
;                                 float u[8], o[8], f[8]; unpack8(ru[j], u);
; #pragma unroll
;                                 for (int i = 0; i < 8; ++i) o[i] = sum[i] * rc - u[i];
;                                 *(u32x4*)(cb + (size_t)t * D + ch0) = pack8(o);
;                                 unpack8(ra[j], f);
; #pragma unroll
;                                 for (int i = 0; i < 8; ++i) sum[i] += fa * f[i];
;                                 unpack8(rb[j], f);
; #pragma unroll
;                                 for (int i = 0; i < 8; ++i) sum[i] -= fb * f[i]; }
	v_lshlrev_b32_e32 v66, 16, v68
	v_and_b32_e32 v67, 0xffff0000, v68
	v_pk_fma_f32 v[152:153], v[32:33], v[70:71], v[90:91] op_sel_hi:[0,1,1]
	v_pk_fma_f32 v[90:91], v[32:33], v[66:67], v[86:87] op_sel_hi:[0,1,1]
	v_lshlrev_b32_e32 v66, 16, v69
	v_and_b32_e32 v67, 0xffff0000, v69
	v_pk_fma_f32 v[84:85], v[32:33], v[66:67], v[76:77] op_sel_hi:[0,1,1]
	v_min_i32_e32 v32, 0x800, v145
	v_sub_u32_e32 v32, v32, v140
	v_cvt_f32_i32_e32 v32, v32
	v_lshlrev_b32_e32 v92, 16, v64
	v_and_b32_e32 v93, 0xffff0000, v64
	v_cndmask_b32_e64 v86, 0, 1.0, vcc
	v_div_scale_f32 v62, s[20:21], v32, v32, 1.0
	v_rcp_f32_e32 v63, v62
	v_lshlrev_b32_e32 v88, 16, v65
	v_and_b32_e32 v89, 0xffff0000, v65
	v_cmp_gt_i32_e64 s[20:21], s39, v145
	v_fma_f32 v64, -v62, v63, 1.0
	v_fmac_f32_e32 v63, v64, v63
	v_div_scale_f32 v64, vcc, 1.0, v32, 1.0
	v_mul_f32_e32 v65, v64, v63
	v_fma_f32 v66, -v62, v65, v64
	v_fmac_f32_e32 v65, v66, v63
	v_fma_f32 v62, -v62, v65, v64
	v_div_fmas_f32 v62, v62, v63, v65
	v_div_fixup_f32 v62, v62, v32, 1.0
	v_min_i32_e32 v32, 0x800, v146
	v_sub_u32_e32 v32, v32, v138
	v_cvt_f32_i32_e32 v32, v32
	v_cmp_lt_i32_e32 vcc, -1, v148
	v_cndmask_b32_e64 v64, 0, 1.0, s[20:21]
	v_lshlrev_b32_e32 v148, 16, v54
	v_and_b32_e32 v149, 0xffff0000, v54
	v_div_scale_f32 v54, s[20:21], v32, v32, 1.0
	v_lshlrev_b32_e32 v144, 16, v55
	v_and_b32_e32 v145, 0xffff0000, v55
	v_rcp_f32_e32 v55, v54
	v_lshlrev_b32_e32 v104, 16, v56
	v_and_b32_e32 v105, 0xffff0000, v56
	v_cndmask_b32_e64 v68, 0, 1.0, vcc
	v_fma_f32 v56, -v54, v55, 1.0
	v_fmac_f32_e32 v55, v56, v55
	v_div_scale_f32 v56, vcc, 1.0, v32, 1.0
	v_lshlrev_b32_e32 v74, 16, v57
	v_and_b32_e32 v75, 0xffff0000, v57
	v_mul_f32_e32 v57, v56, v55
	v_lshlrev_b32_e32 v98, 16, v58
	v_and_b32_e32 v99, 0xffff0000, v58
	v_fma_f32 v58, -v54, v57, v56
	v_fmac_f32_e32 v57, v58, v55
	v_fma_f32 v54, -v54, v57, v56
	v_div_fmas_f32 v54, v54, v55, v57
	v_div_fixup_f32 v58, v54, v32, 1.0
	v_min_i32_e32 v32, 0x800, v156
	v_sub_u32_e32 v32, v32, v106
	v_cvt_f32_i32_e32 v32, v32
	v_cmp_gt_i32_e64 s[20:21], s39, v146
	v_lshlrev_b32_e32 v102, 16, v60
	v_and_b32_e32 v103, 0xffff0000, v60
	v_cndmask_b32_e64 v60, 0, 1.0, s[20:21]
	v_lshlrev_b32_e32 v150, 16, v50
	v_div_scale_f32 v50, s[20:21], v32, v32, 1.0
	v_cmp_lt_i32_e32 vcc, -1, v147
	v_lshlrev_b32_e32 v146, 16, v51
	v_and_b32_e32 v147, 0xffff0000, v51
	v_rcp_f32_e32 v51, v50
	v_lshlrev_b32_e32 v138, 16, v52
	v_and_b32_e32 v139, 0xffff0000, v52
	v_cndmask_b32_e64 v80, 0, 1.0, vcc
	v_fma_f32 v52, -v50, v51, 1.0
	v_fmac_f32_e32 v51, v52, v51
	v_div_scale_f32 v52, vcc, 1.0, v32, 1.0
	v_lshlrev_b32_e32 v82, 16, v53
	v_and_b32_e32 v83, 0xffff0000, v53
	v_mul_f32_e32 v53, v52, v51
	v_fma_f32 v54, -v50, v53, v52
	v_fmac_f32_e32 v53, v54, v51
	v_fma_f32 v50, -v50, v53, v52
	v_div_fmas_f32 v50, v50, v51, v53
	v_div_fixup_f32 v78, v50, v32, 1.0
	v_min_i32_e32 v32, 0x800, v157
	v_sub_u32_e32 v32, v32, v136
	v_cvt_f32_i32_e32 v32, v32
	v_cmp_gt_i32_e64 s[20:21], s39, v156
	v_cmp_lt_i32_e32 vcc, -1, v158
	v_and_b32_e32 v109, 0xffff0000, v46
	v_cndmask_b32_e64 v76, 0, 1.0, s[20:21]
	v_div_scale_f32 v50, s[20:21], v32, v32, 1.0
	v_rcp_f32_e32 v51, v50
	v_cndmask_b32_e64 v72, 0, 1.0, vcc
	v_cmp_gt_i32_e64 s[20:21], s39, v157
	v_lshlrev_b32_e32 v140, 16, v59
	v_fma_f32 v52, -v50, v51, 1.0
	v_fmac_f32_e32 v51, v52, v51
	v_div_scale_f32 v52, vcc, 1.0, v32, 1.0
	v_mul_f32_e32 v53, v52, v51
	v_fma_f32 v54, -v50, v53, v52
	v_fmac_f32_e32 v53, v54, v51
	v_fma_f32 v50, -v50, v53, v52
	v_div_fmas_f32 v50, v50, v51, v53
	v_div_fixup_f32 v70, v50, v32, 1.0
	v_min_i32_e32 v32, 0x800, v107
	v_sub_u32_e32 v32, v32, v108
	v_cvt_f32_i32_e32 v32, v32
	v_cndmask_b32_e64 v56, 0, 1.0, s[20:21]
	v_lshlrev_b32_e32 v108, 16, v46
	v_cmp_lt_i32_e32 vcc, -1, v159
	v_div_scale_f32 v50, s[20:21], v32, v32, 1.0
	v_cmp_gt_i32_e64 s[20:21], s39, v107
	v_pk_fma_f32 v[106:107], v[86:87], v[154:155], v[152:153] op_sel_hi:[0,1,1] neg_lo:[1,0,0] neg_hi:[1,0,0]
	v_pk_fma_f32 v[98:99], v[64:65], v[98:99], v[106:107] op_sel_hi:[0,1,1]
	v_rcp_f32_e32 v51, v50
	v_pk_fma_f32 v[108:109], v[62:63], v[106:107], v[108:109] op_sel_hi:[0,1,1] neg_lo:[0,0,1] neg_hi:[0,0,1]
	v_pk_fma_f32 v[98:99], v[68:69], v[148:149], v[98:99] op_sel_hi:[0,1,1] neg_lo:[1,0,0] neg_hi:[1,0,0]
	v_lshlrev_b32_e32 v106, 16, v42
	v_and_b32_e32 v107, 0xffff0000, v42
	v_pk_fma_f32 v[106:107], v[58:59], v[98:99], v[106:107] op_sel_hi:[0,1,1] neg_lo:[0,0,1] neg_hi:[0,0,1]
	v_cvt_pk_bf16_f32 v42, v106, v107
	v_pk_fma_f32 v[98:99], v[60:61], v[150:151], v[98:99] op_sel_hi:[0,1,1]
	s_waitcnt vmcnt(12)
	v_lshlrev_b32_e32 v106, 16, v34
	v_and_b32_e32 v107, 0xffff0000, v34
	v_pk_fma_f32 v[98:99], v[80:81], v[106:107], v[98:99] op_sel_hi:[0,1,1] neg_lo:[1,0,0] neg_hi:[1,0,0]
	s_waitcnt vmcnt(9)
	v_lshlrev_b32_e32 v106, 16, v38
	v_and_b32_e32 v107, 0xffff0000, v38
	v_fma_f32 v53, -v50, v51, 1.0
	v_pk_fma_f32 v[106:107], v[78:79], v[98:99], v[106:107] op_sel_hi:[0,1,1] neg_lo:[0,0,1] neg_hi:[0,0,1]
	v_cndmask_b32_e64 v52, 0, 1.0, vcc
	v_fmac_f32_e32 v51, v53, v51
	v_div_scale_f32 v53, vcc, 1.0, v32, 1.0
	v_cvt_pk_bf16_f32 v34, v106, v107
	v_lshlrev_b32_e32 v106, 16, v28
	v_and_b32_e32 v107, 0xffff0000, v28
	v_mul_f32_e32 v54, v53, v51
	v_pk_fma_f32 v[98:99], v[76:77], v[106:107], v[98:99] op_sel_hi:[0,1,1]
	v_lshlrev_b32_e32 v106, 16, v24
	v_and_b32_e32 v107, 0xffff0000, v24
	v_fma_f32 v55, -v50, v54, v53
	v_pk_fma_f32 v[98:99], v[72:73], v[106:107], v[98:99] op_sel_hi:[0,1,1] neg_lo:[1,0,0] neg_hi:[1,0,0]
	s_waitcnt vmcnt(8)
	v_lshlrev_b32_e32 v106, 16, v20
	v_and_b32_e32 v107, 0xffff0000, v20
	v_fmac_f32_e32 v54, v55, v51
	v_pk_fma_f32 v[106:107], v[70:71], v[98:99], v[106:107] op_sel_hi:[0,1,1] neg_lo:[0,0,1] neg_hi:[0,0,1]
	v_fma_f32 v50, -v50, v54, v53
	v_cvt_pk_bf16_f32 v20, v106, v107
	s_waitcnt vmcnt(7)
; __device__ __forceinline__ void unpack8(const u32x4 w, float (&f)[8]) { f[0] = bf_lo(w.x); f[1] = bf_hi(w.x); f[2] = bf_lo(w.y); f[3] = bf_hi(w.y); f[4] = bf_lo(w.z); f[5] = bf_hi(w.z); f[6] = bf_lo(w.w); f[7] = bf_hi(w.w); }
; __device__ __forceinline__ u32x4 pack8(const float (&f)[8]) { u32x4 o; o.x = cvt_pk_bf16(f[0], f[1]); o.y = cvt_pk_bf16(f[2], f[3]); o.z = cvt_pk_bf16(f[4], f[5]); o.w = cvt_pk_bf16(f[6], f[7]); return o; }
; __global__ void __launch_bounds__(NWAVES * 64, 2) mk_fwd(Args args) {
;     ...
;                             for (int j = 0; j < 8; ++j) { const int t = tc + j;
;                                 const int wlo = (t - half) > 0 ? (t - half) : 0, whi = (t + half) < SEQ ? (t + half) : SEQ;
;                                 const float rc = 1.0f / (float)(whi - wlo), fa = (t + half < SEQ) ? 1.f : 0.f, fb = (t - half >= 0) ? 1.f : 0.f;
;                                 float u[8], o[8], f[8]; unpack8(ru[j], u);
; #pragma unroll
;                                 for (int i = 0; i < 8; ++i) o[i] = sum[i] * rc - u[i];
;                                 *(u32x4*)(cb + (size_t)t * D + ch0) = pack8(o);
;                                 unpack8(ra[j], f);
; #pragma unroll
;                                 for (int i = 0; i < 8; ++i) sum[i] += fa * f[i];
;                                 unpack8(rb[j], f);
; #pragma unroll
;                                 for (int i = 0; i < 8; ++i) sum[i] -= fb * f[i]; }
	v_lshlrev_b32_e32 v106, 16, v16
	v_and_b32_e32 v107, 0xffff0000, v16
	v_div_fmas_f32 v50, v50, v51, v54
	v_pk_fma_f32 v[98:99], v[56:57], v[106:107], v[98:99] op_sel_hi:[0,1,1]
	s_waitcnt vmcnt(6)
	v_lshlrev_b32_e32 v106, 16, v12
	v_and_b32_e32 v107, 0xffff0000, v12
	v_div_fixup_f32 v54, v50, v32, 1.0
	v_pk_fma_f32 v[98:99], v[52:53], v[106:107], v[98:99] op_sel_hi:[0,1,1] neg_lo:[1,0,0] neg_hi:[1,0,0]
	s_waitcnt vmcnt(5)
	v_lshlrev_b32_e32 v106, 16, v8
	v_and_b32_e32 v107, 0xffff0000, v8
	v_pk_fma_f32 v[106:107], v[54:55], v[98:99], v[106:107] op_sel_hi:[0,1,1] neg_lo:[0,0,1] neg_hi:[0,0,1]
	v_cmp_lt_i32_e32 vcc, -1, v137
	v_cndmask_b32_e64 v50, 0, 1.0, s[20:21]
	v_cvt_pk_bf16_f32 v8, v106, v107
	s_waitcnt vmcnt(4)
	v_lshlrev_b32_e32 v106, 16, v4
	v_and_b32_e32 v107, 0xffff0000, v4
	v_cndmask_b32_e64 v32, 0, 1.0, vcc
	v_pk_fma_f32 v[98:99], v[50:51], v[106:107], v[98:99] op_sel_hi:[0,1,1]
	s_waitcnt vmcnt(3)
	v_lshlrev_b32_e32 v106, 16, v0
	v_and_b32_e32 v107, 0xffff0000, v0
	v_and_b32_e32 v141, 0xffff0000, v59
	v_pk_fma_f32 v[98:99], v[32:33], v[106:107], v[98:99] op_sel_hi:[0,1,1] neg_lo:[1,0,0] neg_hi:[1,0,0]
	v_pk_fma_f32 v[100:101], v[86:87], v[142:143], v[100:101] op_sel_hi:[0,1,1] neg_lo:[1,0,0] neg_hi:[1,0,0]
	v_lshlrev_b32_e32 v106, 16, v47
	v_and_b32_e32 v107, 0xffff0000, v47
	v_pk_fma_f32 v[106:107], v[62:63], v[100:101], v[106:107] op_sel_hi:[0,1,1] neg_lo:[0,0,1] neg_hi:[0,0,1]
	v_pk_fma_f32 v[100:101], v[64:65], v[140:141], v[100:101] op_sel_hi:[0,1,1]
	v_cvt_pk_bf16_f32 v47, v106, v107
	v_pk_fma_f32 v[100:101], v[68:69], v[144:145], v[100:101] op_sel_hi:[0,1,1] neg_lo:[1,0,0] neg_hi:[1,0,0]
	v_lshlrev_b32_e32 v106, 16, v43
	v_and_b32_e32 v107, 0xffff0000, v43
	v_pk_fma_f32 v[106:107], v[58:59], v[100:101], v[106:107] op_sel_hi:[0,1,1] neg_lo:[0,0,1] neg_hi:[0,0,1]
	v_cvt_pk_bf16_f32 v43, v106, v107
	v_pk_fma_f32 v[100:101], v[60:61], v[146:147], v[100:101] op_sel_hi:[0,1,1]
	v_lshlrev_b32_e32 v106, 16, v35
	v_and_b32_e32 v107, 0xffff0000, v35
	v_pk_fma_f32 v[100:101], v[80:81], v[106:107], v[100:101] op_sel_hi:[0,1,1] neg_lo:[1,0,0] neg_hi:[1,0,0]
	v_lshlrev_b32_e32 v28, 16, v29
	v_and_b32_e32 v29, 0xffff0000, v29
	v_pk_fma_f32 v[28:29], v[76:77], v[28:29], v[100:101] op_sel_hi:[0,1,1]
	v_lshlrev_b32_e32 v24, 16, v25
	v_and_b32_e32 v25, 0xffff0000, v25
	v_pk_fma_f32 v[24:25], v[72:73], v[24:25], v[28:29] op_sel_hi:[0,1,1] neg_lo:[1,0,0] neg_hi:[1,0,0]
	v_lshlrev_b32_e32 v16, 16, v17
	v_and_b32_e32 v17, 0xffff0000, v17
	v_pk_fma_f32 v[16:17], v[56:57], v[16:17], v[24:25] op_sel_hi:[0,1,1]
	v_lshlrev_b32_e32 v12, 16, v13
	v_and_b32_e32 v13, 0xffff0000, v13
	v_pk_fma_f32 v[12:13], v[52:53], v[12:13], v[16:17] op_sel_hi:[0,1,1] neg_lo:[1,0,0] neg_hi:[1,0,0]
	v_lshlrev_b32_e32 v4, 16, v5
	v_and_b32_e32 v5, 0xffff0000, v5
	v_lshlrev_b32_e32 v38, 16, v39
	v_and_b32_e32 v39, 0xffff0000, v39
	v_pk_fma_f32 v[4:5], v[50:51], v[4:5], v[12:13] op_sel_hi:[0,1,1]
	v_lshlrev_b32_e32 v0, 16, v1
	v_and_b32_e32 v1, 0xffff0000, v1
	v_pk_fma_f32 v[38:39], v[78:79], v[100:101], v[38:39] op_sel_hi:[0,1,1] neg_lo:[0,0,1] neg_hi:[0,0,1]
	v_pk_fma_f32 v[100:101], v[32:33], v[0:1], v[4:5] op_sel_hi:[0,1,1] neg_lo:[1,0,0] neg_hi:[1,0,0]
	v_pk_fma_f32 v[0:1], v[86:87], v[92:93], v[90:91] op_sel_hi:[0,1,1] neg_lo:[1,0,0] neg_hi:[1,0,0]
	v_lshlrev_b32_e32 v4, 16, v48
	v_and_b32_e32 v5, 0xffff0000, v48
	v_pk_fma_f32 v[4:5], v[62:63], v[0:1], v[4:5] op_sel_hi:[0,1,1] neg_lo:[0,0,1] neg_hi:[0,0,1]
	v_pk_fma_f32 v[0:1], v[64:65], v[102:103], v[0:1] op_sel_hi:[0,1,1]
	v_cvt_pk_bf16_f32 v48, v4, v5
	v_pk_fma_f32 v[0:1], v[68:69], v[104:105], v[0:1] op_sel_hi:[0,1,1] neg_lo:[1,0,0] neg_hi:[1,0,0]
	v_lshlrev_b32_e32 v4, 16, v44
	v_and_b32_e32 v5, 0xffff0000, v44
	v_pk_fma_f32 v[4:5], v[58:59], v[0:1], v[4:5] op_sel_hi:[0,1,1] neg_lo:[0,0,1] neg_hi:[0,0,1]
	v_cvt_pk_bf16_f32 v44, v4, v5
	v_pk_fma_f32 v[0:1], v[60:61], v[138:139], v[0:1] op_sel_hi:[0,1,1]
	v_lshlrev_b32_e32 v4, 16, v36
	v_and_b32_e32 v5, 0xffff0000, v36
	v_pk_fma_f32 v[0:1], v[80:81], v[4:5], v[0:1] op_sel_hi:[0,1,1] neg_lo:[1,0,0] neg_hi:[1,0,0]
	v_lshlrev_b32_e32 v4, 16, v40
	v_and_b32_e32 v5, 0xffff0000, v40
	v_pk_fma_f32 v[4:5], v[78:79], v[0:1], v[4:5] op_sel_hi:[0,1,1] neg_lo:[0,0,1] neg_hi:[0,0,1]
	v_cvt_pk_bf16_f32 v36, v4, v5
	v_lshlrev_b32_e32 v4, 16, v30
	v_and_b32_e32 v5, 0xffff0000, v30
	v_pk_fma_f32 v[0:1], v[76:77], v[4:5], v[0:1] op_sel_hi:[0,1,1]
	v_lshlrev_b32_e32 v4, 16, v26
	v_and_b32_e32 v5, 0xffff0000, v26
; __device__ __forceinline__ void unpack8(const u32x4 w, float (&f)[8]) { f[0] = bf_lo(w.x); f[1] = bf_hi(w.x); f[2] = bf_lo(w.y); f[3] = bf_hi(w.y); f[4] = bf_lo(w.z); f[5] = bf_hi(w.z); f[6] = bf_lo(w.w); f[7] = bf_hi(w.w); }
; __device__ __forceinline__ u32x4 pack8(const float (&f)[8]) { u32x4 o; o.x = cvt_pk_bf16(f[0], f[1]); o.y = cvt_pk_bf16(f[2], f[3]); o.z = cvt_pk_bf16(f[4], f[5]); o.w = cvt_pk_bf16(f[6], f[7]); return o; }
; __global__ void __launch_bounds__(NWAVES * 64, 2) mk_fwd(Args args) {
;     ...
;                         for (int tc = t0; tc < t0 + 32; tc += 8) {
;                             u32x4 ru[8], ra[8], rb[8];
; #pragma unroll
;                             for (int j = 0; j < 8; ++j) { const int t = tc + j, pa = (t + half < SEQ) ? t + half : SEQ - 1, pb = (t - half >= 0) ? t - half : 0;
;                                 ru[j] = *(const u32x4*)(base + (size_t)t * EVEN_IN); ra[j] = *(const u32x4*)(base + (size_t)pa * EVEN_IN); rb[j] = *(const u32x4*)(base + (size_t)pb * EVEN_IN); }
;                             __builtin_amdgcn_sched_barrier(0);
; #pragma unroll
;                             for (int j = 0; j < 8; ++j) { const int t = tc + j;
;                                 const int wlo = (t - half) > 0 ? (t - half) : 0, whi = (t + half) < SEQ ? (t + half) : SEQ;
;                                 const float rc = 1.0f / (float)(whi - wlo), fa = (t + half < SEQ) ? 1.f : 0.f, fb = (t - half >= 0) ? 1.f : 0.f;
;                                 float u[8], o[8], f[8]; unpack8(ru[j], u);
; #pragma unroll
;                                 for (int i = 0; i < 8; ++i) o[i] = sum[i] * rc - u[i];
;                                 *(u32x4*)(cb + (size_t)t * D + ch0) = pack8(o);
;                                 unpack8(ra[j], f);
; #pragma unroll
;                                 for (int i = 0; i < 8; ++i) sum[i] += fa * f[i];
;                                 unpack8(rb[j], f);
; #pragma unroll
;                                 for (int i = 0; i < 8; ++i) sum[i] -= fb * f[i]; }
;                         }
	v_pk_fma_f32 v[0:1], v[72:73], v[4:5], v[0:1] op_sel_hi:[0,1,1] neg_lo:[1,0,0] neg_hi:[1,0,0]
	v_lshlrev_b32_e32 v4, 16, v22
	v_and_b32_e32 v5, 0xffff0000, v22
	v_pk_fma_f32 v[4:5], v[70:71], v[0:1], v[4:5] op_sel_hi:[0,1,1] neg_lo:[0,0,1] neg_hi:[0,0,1]
	v_cvt_pk_bf16_f32 v22, v4, v5
	v_lshlrev_b32_e32 v4, 16, v18
	v_and_b32_e32 v5, 0xffff0000, v18
	v_pk_fma_f32 v[0:1], v[56:57], v[4:5], v[0:1] op_sel_hi:[0,1,1]
	v_lshlrev_b32_e32 v4, 16, v14
	v_and_b32_e32 v5, 0xffff0000, v14
	v_pk_fma_f32 v[0:1], v[52:53], v[4:5], v[0:1] op_sel_hi:[0,1,1] neg_lo:[1,0,0] neg_hi:[1,0,0]
	v_lshlrev_b32_e32 v4, 16, v10
	v_and_b32_e32 v5, 0xffff0000, v10
	v_pk_fma_f32 v[4:5], v[54:55], v[0:1], v[4:5] op_sel_hi:[0,1,1] neg_lo:[0,0,1] neg_hi:[0,0,1]
	v_cvt_pk_bf16_f32 v10, v4, v5
	v_lshlrev_b32_e32 v4, 16, v6
	v_and_b32_e32 v5, 0xffff0000, v6
	v_pk_fma_f32 v[0:1], v[50:51], v[4:5], v[0:1] op_sel_hi:[0,1,1]
	v_lshlrev_b32_e32 v4, 16, v2
	v_and_b32_e32 v5, 0xffff0000, v2
	v_lshlrev_b32_e32 v66, 16, v61
	v_and_b32_e32 v67, 0xffff0000, v61
	v_pk_fma_f32 v[102:103], v[32:33], v[4:5], v[0:1] op_sel_hi:[0,1,1] neg_lo:[1,0,0] neg_hi:[1,0,0]
	v_pk_fma_f32 v[0:1], v[86:87], v[88:89], v[84:85] op_sel_hi:[0,1,1] neg_lo:[1,0,0] neg_hi:[1,0,0]
	v_lshlrev_b32_e32 v4, 16, v49
	v_and_b32_e32 v5, 0xffff0000, v49
	v_pk_fma_f32 v[4:5], v[62:63], v[0:1], v[4:5] op_sel_hi:[0,1,1] neg_lo:[0,0,1] neg_hi:[0,0,1]
	v_pk_fma_f32 v[0:1], v[64:65], v[66:67], v[0:1] op_sel_hi:[0,1,1]
	v_cvt_pk_bf16_f32 v49, v4, v5
	v_pk_fma_f32 v[0:1], v[68:69], v[74:75], v[0:1] op_sel_hi:[0,1,1] neg_lo:[1,0,0] neg_hi:[1,0,0]
	v_lshlrev_b32_e32 v4, 16, v45
	v_and_b32_e32 v5, 0xffff0000, v45
	v_pk_fma_f32 v[4:5], v[58:59], v[0:1], v[4:5] op_sel_hi:[0,1,1] neg_lo:[0,0,1] neg_hi:[0,0,1]
	v_cvt_pk_bf16_f32 v45, v4, v5
	v_pk_fma_f32 v[0:1], v[60:61], v[82:83], v[0:1] op_sel_hi:[0,1,1]
	v_lshlrev_b32_e32 v4, 16, v37
	v_and_b32_e32 v5, 0xffff0000, v37
	v_pk_fma_f32 v[0:1], v[80:81], v[4:5], v[0:1] op_sel_hi:[0,1,1] neg_lo:[1,0,0] neg_hi:[1,0,0]
	v_lshlrev_b32_e32 v4, 16, v41
	v_and_b32_e32 v5, 0xffff0000, v41
	v_pk_fma_f32 v[4:5], v[78:79], v[0:1], v[4:5] op_sel_hi:[0,1,1] neg_lo:[0,0,1] neg_hi:[0,0,1]
	v_cvt_pk_bf16_f32 v37, v4, v5
	v_lshlrev_b32_e32 v4, 16, v31
	v_and_b32_e32 v5, 0xffff0000, v31
	v_pk_fma_f32 v[0:1], v[76:77], v[4:5], v[0:1] op_sel_hi:[0,1,1]
	v_lshlrev_b32_e32 v4, 16, v27
	v_and_b32_e32 v5, 0xffff0000, v27
	v_pk_fma_f32 v[0:1], v[72:73], v[4:5], v[0:1] op_sel_hi:[0,1,1] neg_lo:[1,0,0] neg_hi:[1,0,0]
	v_lshlrev_b32_e32 v4, 16, v23
	v_and_b32_e32 v5, 0xffff0000, v23
	v_pk_fma_f32 v[4:5], v[70:71], v[0:1], v[4:5] op_sel_hi:[0,1,1] neg_lo:[0,0,1] neg_hi:[0,0,1]
	v_cvt_pk_bf16_f32 v23, v4, v5
	v_lshlrev_b32_e32 v4, 16, v19
	v_and_b32_e32 v5, 0xffff0000, v19
	v_pk_fma_f32 v[0:1], v[56:57], v[4:5], v[0:1] op_sel_hi:[0,1,1]
	v_lshlrev_b32_e32 v4, 16, v15
	v_and_b32_e32 v5, 0xffff0000, v15
	v_pk_fma_f32 v[0:1], v[52:53], v[4:5], v[0:1] op_sel_hi:[0,1,1] neg_lo:[1,0,0] neg_hi:[1,0,0]
	v_lshlrev_b32_e32 v4, 16, v11
	v_and_b32_e32 v5, 0xffff0000, v11
	v_pk_fma_f32 v[4:5], v[54:55], v[0:1], v[4:5] op_sel_hi:[0,1,1] neg_lo:[0,0,1] neg_hi:[0,0,1]
	v_cvt_pk_bf16_f32 v11, v4, v5
	v_lshlrev_b32_e32 v4, 16, v7
	v_and_b32_e32 v5, 0xffff0000, v7
	v_pk_fma_f32 v[0:1], v[50:51], v[4:5], v[0:1] op_sel_hi:[0,1,1]
	v_add_co_u32_e32 v4, vcc, s34, v94
	s_addc_u32 s23, s23, 0
	s_nop 0
	v_addc_co_u32_e32 v5, vcc, 0, v95, vcc
	s_add_u32 s24, s24, 0x8000
	v_lshlrev_b32_e32 v28, 16, v21
	v_and_b32_e32 v29, 0xffff0000, v21
	v_lshlrev_b32_e32 v16, 16, v9
	v_and_b32_e32 v17, 0xffff0000, v9
	v_lshlrev_b32_e32 v2, 16, v3
	v_and_b32_e32 v3, 0xffff0000, v3
	v_add_co_u32_e32 v6, vcc, s35, v94
	s_addc_u32 s25, s25, 0
	v_cvt_pk_bf16_f32 v46, v108, v109
	v_pk_fma_f32 v[28:29], v[70:71], v[24:25], v[28:29] op_sel_hi:[0,1,1] neg_lo:[0,0,1] neg_hi:[0,0,1]
	v_pk_fma_f32 v[16:17], v[54:55], v[12:13], v[16:17] op_sel_hi:[0,1,1] neg_lo:[0,0,1] neg_hi:[0,0,1]
	v_addc_co_u32_e32 v7, vcc, 0, v95, vcc
	v_pk_fma_f32 v[104:105], v[32:33], v[2:3], v[0:1] op_sel_hi:[0,1,1] neg_lo:[1,0,0] neg_hi:[1,0,0]
	s_cmp_ge_u32 s30, s18
	v_cvt_pk_bf16_f32 v35, v38, v39
	v_cvt_pk_bf16_f32 v21, v28, v29
	v_cvt_pk_bf16_f32 v9, v16, v17
	global_store_dwordx4 v[96:97], v[46:49], off offset:2048
	global_store_dwordx4 v[6:7], v[42:45], off offset:-4096
	global_store_dwordx4 v[4:5], v[34:37], off offset:2048
	global_store_dwordx4 v[6:7], v[20:23], off
	global_store_dwordx4 v[6:7], v[8:11], off offset:2048
	s_cbranch_scc0 .LBB0_368
	s_branch .LBB0_358
